# g3 + GEMM K-loops (A, K/V proj, C, F): LDS-DMA tile loads issued before the ds_read burst in each load segment
# baseline (speedup 1.0000x reference)
.LBB0_198:
	s_add_u32 s20, s18, 0xfff80080
	s_addc_u32 s21, s19, -1
	s_add_i32 s49, 0, 0x10000
	s_cmp_eq_u32 s48, 28
	s_cselect_b32 s23, s15, s21
	s_cselect_b32 s22, s14, s20
	s_cselect_b32 s21, s17, s46
	s_cselect_b32 s20, s16, s3
	s_add_i32 s60, 0, 0x14000
	v_lshl_add_u64 v[194:195], s[18:19], 0, v[144:145]
	s_add_i32 m0, s34, 0xc000
	s_nop 0
	global_load_lds_dwordx4 v[194:195], off
	v_lshl_add_u64 v[194:195], s[18:19], 0, v[142:143]
	s_add_i32 m0, s34, 0xe000
	s_nop 0
	global_load_lds_dwordx4 v[194:195], off
	v_add_u32_e32 v2, s49, v1
	ds_read_b128 v[146:149], v2
	ds_read_b128 v[150:153], v2 offset:1024
	ds_read_b128 v[154:157], v2 offset:2048
	ds_read_b128 v[158:161], v2 offset:3072
	v_add_u32_e32 v2, s60, v1
	ds_read_b128 v[162:165], v2
	ds_read_b128 v[166:169], v2 offset:1024
	ds_read_b128 v[170:173], v2 offset:2048
	ds_read_b128 v[174:177], v2 offset:3072
	ds_read_b128 v[178:181], v133
	ds_read_b128 v[182:185], v133 offset:1024
	ds_read_b128 v[186:189], v133 offset:2048
	ds_read_b128 v[190:193], v133 offset:3072
	ds_read_b128 v[204:207], v133 offset:4096
	ds_read_b128 v[208:211], v133 offset:5120
	ds_read_b128 v[212:215], v133 offset:6144
	ds_read_b128 v[226:229], v133 offset:7168
	s_waitcnt vmcnt(8)
	s_waitcnt lgkmcnt(0)
	s_barrier
	s_setprio 1
	s_waitcnt lgkmcnt(0)
	v_mfma_f32_16x16x32_bf16 v[128:131], v[146:149], v[178:181], v[128:131]
	v_mfma_f32_16x16x32_bf16 v[124:127], v[154:157], v[178:181], v[124:127]
	v_mfma_f32_16x16x32_bf16 v[112:115], v[146:149], v[186:189], v[112:115]
	v_mfma_f32_16x16x32_bf16 v[108:111], v[154:157], v[186:189], v[108:111]
	v_mfma_f32_16x16x32_bf16 v[96:99], v[146:149], v[204:207], v[96:99]
	v_mfma_f32_16x16x32_bf16 v[92:95], v[154:157], v[204:207], v[92:95]
	v_mfma_f32_16x16x32_bf16 v[80:83], v[146:149], v[212:215], v[80:83]
	v_mfma_f32_16x16x32_bf16 v[76:79], v[154:157], v[212:215], v[76:79]
	v_mfma_f32_16x16x32_bf16 v[128:131], v[150:153], v[182:185], v[128:131]
	v_mfma_f32_16x16x32_bf16 v[124:127], v[158:161], v[182:185], v[124:127]
	v_mfma_f32_16x16x32_bf16 v[112:115], v[150:153], v[190:193], v[112:115]
	v_mfma_f32_16x16x32_bf16 v[108:111], v[158:161], v[190:193], v[108:111]
	v_mfma_f32_16x16x32_bf16 v[96:99], v[150:153], v[208:211], v[96:99]
	v_mfma_f32_16x16x32_bf16 v[92:95], v[158:161], v[208:211], v[92:95]
	v_mfma_f32_16x16x32_bf16 v[80:83], v[150:153], v[226:229], v[80:83]
	v_mfma_f32_16x16x32_bf16 v[76:79], v[158:161], v[226:229], v[76:79]
	s_setprio 0
	s_setprio 1
	v_mfma_f32_16x16x32_bf16 v[120:123], v[162:165], v[178:181], v[120:123]
	v_mfma_f32_16x16x32_bf16 v[116:119], v[170:173], v[178:181], v[116:119]
	v_mfma_f32_16x16x32_bf16 v[104:107], v[162:165], v[186:189], v[104:107]
	v_mfma_f32_16x16x32_bf16 v[100:103], v[170:173], v[186:189], v[100:103]
	v_mfma_f32_16x16x32_bf16 v[88:91], v[162:165], v[204:207], v[88:91]
	v_mfma_f32_16x16x32_bf16 v[84:87], v[170:173], v[204:207], v[84:87]
	v_mfma_f32_16x16x32_bf16 v[72:75], v[162:165], v[212:215], v[72:75]
	v_mfma_f32_16x16x32_bf16 v[68:71], v[170:173], v[212:215], v[68:71]
	v_mfma_f32_16x16x32_bf16 v[120:123], v[166:169], v[182:185], v[120:123]
	v_mfma_f32_16x16x32_bf16 v[116:119], v[174:177], v[182:185], v[116:119]
	v_mfma_f32_16x16x32_bf16 v[104:107], v[166:169], v[190:193], v[104:107]
	v_mfma_f32_16x16x32_bf16 v[100:103], v[174:177], v[190:193], v[100:103]
	v_mfma_f32_16x16x32_bf16 v[88:91], v[166:169], v[208:211], v[88:91]
	v_mfma_f32_16x16x32_bf16 v[84:87], v[174:177], v[208:211], v[84:87]
	v_mfma_f32_16x16x32_bf16 v[72:75], v[166:169], v[226:229], v[72:75]
	v_mfma_f32_16x16x32_bf16 v[68:71], v[174:177], v[226:229], v[68:71]
	s_setprio 0
	s_barrier
	s_add_i32 s49, s49, s31
	v_lshl_add_u64 v[194:195], s[20:21], 0, v[134:135]
	s_mov_b32 m0, s49
	s_nop 0
	global_load_lds_dwordx4 v[194:195], off
	s_add_i32 m0, s49, 0x2000
	s_add_u32 s58, s20, 0x80000
	v_lshl_add_u64 v[230:231], s[20:21], 0, v[138:139]
	s_addc_u32 s59, s21, 0
	s_add_i32 s49, s60, s31
	global_load_lds_dwordx4 v[230:231], off
	v_lshl_add_u64 v[232:233], s[58:59], 0, v[134:135]
	s_mov_b32 m0, s49
	v_lshl_add_u64 v[234:235], s[22:23], 0, v[140:141]
	global_load_lds_dwordx4 v[232:233], off
	v_lshl_add_u64 v[232:233], s[58:59], 0, v[138:139]
	s_add_i32 m0, s49, 0x2000
	s_nop 0
	global_load_lds_dwordx4 v[232:233], off
	v_lshl_add_u64 v[232:233], s[22:23], 0, v[136:137]
	s_mov_b32 m0, s34
	s_nop 0
	global_load_lds_dwordx4 v[232:233], off
	s_mov_b32 m0, s35
	s_nop 0
	global_load_lds_dwordx4 v[234:235], off
	ds_read_b128 v[178:181], v133 offset:16384
	ds_read_b128 v[182:185], v133 offset:17408
	ds_read_b128 v[186:189], v133 offset:18432
	ds_read_b128 v[190:193], v133 offset:19456
	ds_read_b128 v[204:207], v133 offset:20480
	ds_read_b128 v[208:211], v133 offset:21504
	ds_read_b128 v[212:215], v133 offset:22528
	ds_read_b128 v[226:229], v133 offset:23552
	s_waitcnt vmcnt(8)
	s_waitcnt lgkmcnt(0)
	s_barrier
	s_setprio 1
	s_waitcnt lgkmcnt(0)
	v_mfma_f32_16x16x32_bf16 v[64:67], v[146:149], v[178:181], v[64:67]
	v_mfma_f32_16x16x32_bf16 v[60:63], v[154:157], v[178:181], v[60:63]
	v_mfma_f32_16x16x32_bf16 v[48:51], v[146:149], v[186:189], v[48:51]
	v_mfma_f32_16x16x32_bf16 v[44:47], v[154:157], v[186:189], v[44:47]
	v_mfma_f32_16x16x32_bf16 v[32:35], v[146:149], v[204:207], v[32:35]
	v_mfma_f32_16x16x32_bf16 v[28:31], v[154:157], v[204:207], v[28:31]
	v_mfma_f32_16x16x32_bf16 v[16:19], v[146:149], v[212:215], v[16:19]
	v_mfma_f32_16x16x32_bf16 v[12:15], v[154:157], v[212:215], v[12:15]
	v_mfma_f32_16x16x32_bf16 v[64:67], v[150:153], v[182:185], v[64:67]
	v_mfma_f32_16x16x32_bf16 v[60:63], v[158:161], v[182:185], v[60:63]
	v_mfma_f32_16x16x32_bf16 v[48:51], v[150:153], v[190:193], v[48:51]
	v_mfma_f32_16x16x32_bf16 v[44:47], v[158:161], v[190:193], v[44:47]
	v_mfma_f32_16x16x32_bf16 v[32:35], v[150:153], v[208:211], v[32:35]
	v_mfma_f32_16x16x32_bf16 v[28:31], v[158:161], v[208:211], v[28:31]
	v_mfma_f32_16x16x32_bf16 v[16:19], v[150:153], v[226:229], v[16:19]
	v_mfma_f32_16x16x32_bf16 v[12:15], v[158:161], v[226:229], v[12:15]
	s_setprio 0
	s_setprio 1
	v_mfma_f32_16x16x32_bf16 v[56:59], v[162:165], v[178:181], v[56:59]
	v_mfma_f32_16x16x32_bf16 v[52:55], v[170:173], v[178:181], v[52:55]
	v_mfma_f32_16x16x32_bf16 v[40:43], v[162:165], v[186:189], v[40:43]
	v_mfma_f32_16x16x32_bf16 v[36:39], v[170:173], v[186:189], v[36:39]
	v_mfma_f32_16x16x32_bf16 v[24:27], v[162:165], v[204:207], v[24:27]
	v_mfma_f32_16x16x32_bf16 v[20:23], v[170:173], v[204:207], v[20:23]
	v_mfma_f32_16x16x32_bf16 v[8:11], v[162:165], v[212:215], v[8:11]
	v_mfma_f32_16x16x32_bf16 v[4:7], v[170:173], v[212:215], v[4:7]
	v_mfma_f32_16x16x32_bf16 v[56:59], v[166:169], v[182:185], v[56:59]
	v_mfma_f32_16x16x32_bf16 v[52:55], v[174:177], v[182:185], v[52:55]
	v_mfma_f32_16x16x32_bf16 v[40:43], v[166:169], v[190:193], v[40:43]
	v_mfma_f32_16x16x32_bf16 v[36:39], v[174:177], v[190:193], v[36:39]
	v_mfma_f32_16x16x32_bf16 v[24:27], v[166:169], v[208:211], v[24:27]
	v_mfma_f32_16x16x32_bf16 v[20:23], v[174:177], v[208:211], v[20:23]
	v_mfma_f32_16x16x32_bf16 v[8:11], v[166:169], v[226:229], v[8:11]
	v_mfma_f32_16x16x32_bf16 v[4:7], v[174:177], v[226:229], v[4:7]
	s_setprio 0
	s_barrier
	s_add_i32 s49, 0, 0x18000
	s_add_i32 s58, 0, 0x1c000
	s_add_u32 s22, s22, 0x80000
	s_addc_u32 s23, s23, 0
	s_mov_b32 m0, s36
	v_lshl_add_u64 v[236:237], s[22:23], 0, v[136:137]
	global_load_lds_dwordx4 v[236:237], off
	v_lshl_add_u64 v[236:237], s[22:23], 0, v[140:141]
	s_mov_b32 m0, s37
	s_nop 0
	global_load_lds_dwordx4 v[236:237], off
	v_add_u32_e32 v2, s49, v1
	ds_read_b128 v[146:149], v2
	ds_read_b128 v[150:153], v2 offset:1024
	ds_read_b128 v[154:157], v2 offset:2048
	ds_read_b128 v[158:161], v2 offset:3072
	v_add_u32_e32 v2, s58, v1
	ds_read_b128 v[162:165], v2
	ds_read_b128 v[166:169], v2 offset:1024
	ds_read_b128 v[170:173], v2 offset:2048
	ds_read_b128 v[174:177], v2 offset:3072
	ds_read_b128 v[178:181], v133 offset:32768
	ds_read_b128 v[182:185], v133 offset:33792
	ds_read_b128 v[186:189], v133 offset:34816
	ds_read_b128 v[190:193], v133 offset:35840
	ds_read_b128 v[204:207], v133 offset:36864
	ds_read_b128 v[208:211], v133 offset:37888
	ds_read_b128 v[212:215], v133 offset:38912
	ds_read_b128 v[226:229], v133 offset:39936
	s_waitcnt vmcnt(8)
	s_waitcnt lgkmcnt(0)
	s_barrier
	s_setprio 1
	s_waitcnt lgkmcnt(0)
	v_mfma_f32_16x16x32_bf16 v[128:131], v[146:149], v[178:181], v[128:131]
	v_mfma_f32_16x16x32_bf16 v[124:127], v[154:157], v[178:181], v[124:127]
	v_mfma_f32_16x16x32_bf16 v[112:115], v[146:149], v[186:189], v[112:115]
	v_mfma_f32_16x16x32_bf16 v[108:111], v[154:157], v[186:189], v[108:111]
	v_mfma_f32_16x16x32_bf16 v[96:99], v[146:149], v[204:207], v[96:99]
	v_mfma_f32_16x16x32_bf16 v[92:95], v[154:157], v[204:207], v[92:95]
	v_mfma_f32_16x16x32_bf16 v[80:83], v[146:149], v[212:215], v[80:83]
	v_mfma_f32_16x16x32_bf16 v[76:79], v[154:157], v[212:215], v[76:79]
	v_mfma_f32_16x16x32_bf16 v[128:131], v[150:153], v[182:185], v[128:131]
	v_mfma_f32_16x16x32_bf16 v[124:127], v[158:161], v[182:185], v[124:127]
	v_mfma_f32_16x16x32_bf16 v[112:115], v[150:153], v[190:193], v[112:115]
	v_mfma_f32_16x16x32_bf16 v[108:111], v[158:161], v[190:193], v[108:111]
	v_mfma_f32_16x16x32_bf16 v[96:99], v[150:153], v[208:211], v[96:99]
	v_mfma_f32_16x16x32_bf16 v[92:95], v[158:161], v[208:211], v[92:95]
	v_mfma_f32_16x16x32_bf16 v[80:83], v[150:153], v[226:229], v[80:83]
	v_mfma_f32_16x16x32_bf16 v[76:79], v[158:161], v[226:229], v[76:79]
	s_setprio 0
	s_setprio 1
	v_mfma_f32_16x16x32_bf16 v[120:123], v[162:165], v[178:181], v[120:123]
	v_mfma_f32_16x16x32_bf16 v[116:119], v[170:173], v[178:181], v[116:119]
	v_mfma_f32_16x16x32_bf16 v[104:107], v[162:165], v[186:189], v[104:107]
	v_mfma_f32_16x16x32_bf16 v[100:103], v[170:173], v[186:189], v[100:103]
	v_mfma_f32_16x16x32_bf16 v[88:91], v[162:165], v[204:207], v[88:91]
	v_mfma_f32_16x16x32_bf16 v[84:87], v[170:173], v[204:207], v[84:87]
	v_mfma_f32_16x16x32_bf16 v[72:75], v[162:165], v[212:215], v[72:75]
	v_mfma_f32_16x16x32_bf16 v[68:71], v[170:173], v[212:215], v[68:71]
	v_mfma_f32_16x16x32_bf16 v[120:123], v[166:169], v[182:185], v[120:123]
	v_mfma_f32_16x16x32_bf16 v[116:119], v[174:177], v[182:185], v[116:119]
	v_mfma_f32_16x16x32_bf16 v[104:107], v[166:169], v[190:193], v[104:107]
	v_mfma_f32_16x16x32_bf16 v[100:103], v[174:177], v[190:193], v[100:103]
	v_mfma_f32_16x16x32_bf16 v[88:91], v[166:169], v[208:211], v[88:91]
	v_mfma_f32_16x16x32_bf16 v[84:87], v[174:177], v[208:211], v[84:87]
	v_mfma_f32_16x16x32_bf16 v[72:75], v[166:169], v[226:229], v[72:75]
	v_mfma_f32_16x16x32_bf16 v[68:71], v[174:177], v[226:229], v[68:71]
	s_setprio 0
	s_barrier
	s_add_i32 s22, s49, s31
	v_lshl_add_u64 v[194:195], v[194:195], 0, s[94:95]
	s_mov_b32 m0, s22
	s_nop 0
	global_load_lds_dwordx4 v[194:195], off
	s_add_i32 m0, s22, 0x2000
	s_add_u32 s20, s20, 0x80080
	v_lshl_add_u64 v[194:195], v[230:231], 0, s[94:95]
	s_addc_u32 s21, s21, 0
	s_add_i32 s22, s58, s31
	global_load_lds_dwordx4 v[194:195], off
	v_lshl_add_u64 v[194:195], s[20:21], 0, v[134:135]
	s_mov_b32 m0, s22
	s_nop 0
	global_load_lds_dwordx4 v[194:195], off
	v_lshl_add_u64 v[194:195], s[20:21], 0, v[138:139]
	s_add_i32 m0, s22, 0x2000
	s_nop 0
	global_load_lds_dwordx4 v[194:195], off
	v_lshl_add_u64 v[194:195], v[232:233], 0, s[94:95]
	s_mov_b32 m0, s40
	s_nop 0
	global_load_lds_dwordx4 v[194:195], off
	v_lshl_add_u64 v[194:195], v[234:235], 0, s[94:95]
	s_mov_b32 m0, s41
	s_nop 0
	global_load_lds_dwordx4 v[194:195], off
	ds_read_b128 v[178:181], v133 offset:49152
	ds_read_b128 v[182:185], v133 offset:50176
	ds_read_b128 v[186:189], v133 offset:51200
	ds_read_b128 v[190:193], v133 offset:52224
	ds_read_b128 v[204:207], v133 offset:53248
	ds_read_b128 v[208:211], v133 offset:54272
	ds_read_b128 v[212:215], v133 offset:55296
	ds_read_b128 v[226:229], v133 offset:56320
	s_waitcnt vmcnt(8)
	s_waitcnt lgkmcnt(0)
	s_barrier
	s_setprio 1
	s_waitcnt lgkmcnt(0)
	v_mfma_f32_16x16x32_bf16 v[64:67], v[146:149], v[178:181], v[64:67]
	v_mfma_f32_16x16x32_bf16 v[60:63], v[154:157], v[178:181], v[60:63]
	v_mfma_f32_16x16x32_bf16 v[48:51], v[146:149], v[186:189], v[48:51]
	v_mfma_f32_16x16x32_bf16 v[44:47], v[154:157], v[186:189], v[44:47]
	v_mfma_f32_16x16x32_bf16 v[32:35], v[146:149], v[204:207], v[32:35]
	v_mfma_f32_16x16x32_bf16 v[28:31], v[154:157], v[204:207], v[28:31]
	v_mfma_f32_16x16x32_bf16 v[16:19], v[146:149], v[212:215], v[16:19]
	v_mfma_f32_16x16x32_bf16 v[12:15], v[154:157], v[212:215], v[12:15]
	v_mfma_f32_16x16x32_bf16 v[64:67], v[150:153], v[182:185], v[64:67]
	v_mfma_f32_16x16x32_bf16 v[60:63], v[158:161], v[182:185], v[60:63]
	v_mfma_f32_16x16x32_bf16 v[48:51], v[150:153], v[190:193], v[48:51]
	v_mfma_f32_16x16x32_bf16 v[44:47], v[158:161], v[190:193], v[44:47]
	v_mfma_f32_16x16x32_bf16 v[32:35], v[150:153], v[208:211], v[32:35]
	v_mfma_f32_16x16x32_bf16 v[28:31], v[158:161], v[208:211], v[28:31]
	v_mfma_f32_16x16x32_bf16 v[16:19], v[150:153], v[226:229], v[16:19]
	v_mfma_f32_16x16x32_bf16 v[12:15], v[158:161], v[226:229], v[12:15]
	s_setprio 0
	s_setprio 1
	v_mfma_f32_16x16x32_bf16 v[56:59], v[162:165], v[178:181], v[56:59]
	v_mfma_f32_16x16x32_bf16 v[52:55], v[170:173], v[178:181], v[52:55]
	v_mfma_f32_16x16x32_bf16 v[40:43], v[162:165], v[186:189], v[40:43]
	v_mfma_f32_16x16x32_bf16 v[36:39], v[170:173], v[186:189], v[36:39]
	v_mfma_f32_16x16x32_bf16 v[24:27], v[162:165], v[204:207], v[24:27]
	v_mfma_f32_16x16x32_bf16 v[20:23], v[170:173], v[204:207], v[20:23]
	v_mfma_f32_16x16x32_bf16 v[8:11], v[162:165], v[212:215], v[8:11]
	v_mfma_f32_16x16x32_bf16 v[4:7], v[170:173], v[212:215], v[4:7]
	v_mfma_f32_16x16x32_bf16 v[56:59], v[166:169], v[182:185], v[56:59]
	v_mfma_f32_16x16x32_bf16 v[52:55], v[174:177], v[182:185], v[52:55]
	v_mfma_f32_16x16x32_bf16 v[40:43], v[166:169], v[190:193], v[40:43]
	v_mfma_f32_16x16x32_bf16 v[36:39], v[174:177], v[190:193], v[36:39]
	v_mfma_f32_16x16x32_bf16 v[24:27], v[166:169], v[208:211], v[24:27]
	v_mfma_f32_16x16x32_bf16 v[20:23], v[174:177], v[208:211], v[20:23]
	v_mfma_f32_16x16x32_bf16 v[8:11], v[166:169], v[226:229], v[8:11]
	v_mfma_f32_16x16x32_bf16 v[4:7], v[174:177], v[226:229], v[4:7]
	s_setprio 0
	s_barrier
	s_add_i32 s48, s48, 2
	s_add_u32 s3, s3, 0x100
	s_addc_u32 s46, s46, 0
	s_add_u32 s18, s18, 0x100
	s_addc_u32 s19, s19, 0
	s_cmp_gt_u32 s48, 29
	s_cbranch_scc0 .LBB0_198
	s_and_b64 vcc, exec, s[10:11]
	s_cbranch_vccz .LBB0_201
	s_barrier

.LBB0_236:
	s_add_u32 s20, s18, 0xfff80080
	s_addc_u32 s21, s19, -1
	s_add_i32 s58, 0, 0x10000
	s_cmp_eq_u32 s49, 28
	s_cselect_b32 s23, s15, s21
	s_cselect_b32 s22, s14, s20
	s_cselect_b32 s21, s17, s46
	s_cselect_b32 s20, s16, s3
	s_add_i32 s60, 0, 0x14000
	v_lshl_add_u64 v[194:195], s[18:19], 0, v[144:145]
	s_add_i32 m0, s35, 0xc000
	s_nop 0
	global_load_lds_dwordx4 v[194:195], off
	v_lshl_add_u64 v[194:195], s[18:19], 0, v[142:143]
	s_add_i32 m0, s35, 0xe000
	s_nop 0
	global_load_lds_dwordx4 v[194:195], off
	v_add_u32_e32 v2, s58, v1
	ds_read_b128 v[146:149], v2
	ds_read_b128 v[150:153], v2 offset:1024
	ds_read_b128 v[154:157], v2 offset:2048
	ds_read_b128 v[158:161], v2 offset:3072
	v_add_u32_e32 v2, s60, v1
	ds_read_b128 v[162:165], v2
	ds_read_b128 v[166:169], v2 offset:1024
	ds_read_b128 v[170:173], v2 offset:2048
	ds_read_b128 v[174:177], v2 offset:3072
	ds_read_b128 v[178:181], v133
	ds_read_b128 v[182:185], v133 offset:1024
	ds_read_b128 v[186:189], v133 offset:2048
	ds_read_b128 v[190:193], v133 offset:3072
	ds_read_b128 v[204:207], v133 offset:4096
	ds_read_b128 v[208:211], v133 offset:5120
	ds_read_b128 v[212:215], v133 offset:6144
	ds_read_b128 v[226:229], v133 offset:7168
	s_waitcnt vmcnt(8)
	s_waitcnt lgkmcnt(0)
	s_barrier
	s_setprio 1
	s_waitcnt lgkmcnt(0)
	v_mfma_f32_16x16x32_bf16 v[128:131], v[146:149], v[178:181], v[128:131]
	v_mfma_f32_16x16x32_bf16 v[124:127], v[154:157], v[178:181], v[124:127]
	v_mfma_f32_16x16x32_bf16 v[112:115], v[146:149], v[186:189], v[112:115]
	v_mfma_f32_16x16x32_bf16 v[108:111], v[154:157], v[186:189], v[108:111]
	v_mfma_f32_16x16x32_bf16 v[96:99], v[146:149], v[204:207], v[96:99]
	v_mfma_f32_16x16x32_bf16 v[92:95], v[154:157], v[204:207], v[92:95]
	v_mfma_f32_16x16x32_bf16 v[80:83], v[146:149], v[212:215], v[80:83]
	v_mfma_f32_16x16x32_bf16 v[76:79], v[154:157], v[212:215], v[76:79]
	v_mfma_f32_16x16x32_bf16 v[128:131], v[150:153], v[182:185], v[128:131]
	v_mfma_f32_16x16x32_bf16 v[124:127], v[158:161], v[182:185], v[124:127]
	v_mfma_f32_16x16x32_bf16 v[112:115], v[150:153], v[190:193], v[112:115]
	v_mfma_f32_16x16x32_bf16 v[108:111], v[158:161], v[190:193], v[108:111]
	v_mfma_f32_16x16x32_bf16 v[96:99], v[150:153], v[208:211], v[96:99]
	v_mfma_f32_16x16x32_bf16 v[92:95], v[158:161], v[208:211], v[92:95]
	v_mfma_f32_16x16x32_bf16 v[80:83], v[150:153], v[226:229], v[80:83]
	v_mfma_f32_16x16x32_bf16 v[76:79], v[158:161], v[226:229], v[76:79]
	s_setprio 0
	s_setprio 1
	v_mfma_f32_16x16x32_bf16 v[120:123], v[162:165], v[178:181], v[120:123]
	v_mfma_f32_16x16x32_bf16 v[116:119], v[170:173], v[178:181], v[116:119]
	v_mfma_f32_16x16x32_bf16 v[104:107], v[162:165], v[186:189], v[104:107]
	v_mfma_f32_16x16x32_bf16 v[100:103], v[170:173], v[186:189], v[100:103]
	v_mfma_f32_16x16x32_bf16 v[88:91], v[162:165], v[204:207], v[88:91]
	v_mfma_f32_16x16x32_bf16 v[84:87], v[170:173], v[204:207], v[84:87]
	v_mfma_f32_16x16x32_bf16 v[72:75], v[162:165], v[212:215], v[72:75]
	v_mfma_f32_16x16x32_bf16 v[68:71], v[170:173], v[212:215], v[68:71]
	v_mfma_f32_16x16x32_bf16 v[120:123], v[166:169], v[182:185], v[120:123]
	v_mfma_f32_16x16x32_bf16 v[116:119], v[174:177], v[182:185], v[116:119]
	v_mfma_f32_16x16x32_bf16 v[104:107], v[166:169], v[190:193], v[104:107]
	v_mfma_f32_16x16x32_bf16 v[100:103], v[174:177], v[190:193], v[100:103]
	v_mfma_f32_16x16x32_bf16 v[88:91], v[166:169], v[208:211], v[88:91]
	v_mfma_f32_16x16x32_bf16 v[84:87], v[174:177], v[208:211], v[84:87]
	v_mfma_f32_16x16x32_bf16 v[72:75], v[166:169], v[226:229], v[72:75]
	v_mfma_f32_16x16x32_bf16 v[68:71], v[174:177], v[226:229], v[68:71]
	s_setprio 0
	s_barrier
	s_add_i32 s58, s58, s34
	v_lshl_add_u64 v[194:195], s[20:21], 0, v[134:135]
	s_mov_b32 m0, s58
	s_nop 0
	global_load_lds_dwordx4 v[194:195], off
	s_add_i32 m0, s58, 0x2000
	s_add_u32 s58, s20, 0x80000
	v_lshl_add_u64 v[230:231], s[20:21], 0, v[138:139]
	s_addc_u32 s59, s21, 0
	s_add_i32 s60, s60, s34
	global_load_lds_dwordx4 v[230:231], off
	v_lshl_add_u64 v[232:233], s[58:59], 0, v[134:135]
	s_mov_b32 m0, s60
	v_lshl_add_u64 v[234:235], s[22:23], 0, v[140:141]
	global_load_lds_dwordx4 v[232:233], off
	v_lshl_add_u64 v[232:233], s[58:59], 0, v[138:139]
	s_add_i32 m0, s60, 0x2000
	s_nop 0
	global_load_lds_dwordx4 v[232:233], off
	v_lshl_add_u64 v[232:233], s[22:23], 0, v[136:137]
	s_mov_b32 m0, s35
	s_nop 0
	global_load_lds_dwordx4 v[232:233], off
	s_mov_b32 m0, s36
	s_nop 0
	global_load_lds_dwordx4 v[234:235], off
	ds_read_b128 v[178:181], v133 offset:16384
	ds_read_b128 v[182:185], v133 offset:17408
	ds_read_b128 v[186:189], v133 offset:18432
	ds_read_b128 v[190:193], v133 offset:19456
	ds_read_b128 v[204:207], v133 offset:20480
	ds_read_b128 v[208:211], v133 offset:21504
	ds_read_b128 v[212:215], v133 offset:22528
	ds_read_b128 v[226:229], v133 offset:23552
	s_waitcnt vmcnt(8)
	s_waitcnt lgkmcnt(0)
	s_barrier
	s_setprio 1
	s_waitcnt lgkmcnt(0)
	v_mfma_f32_16x16x32_bf16 v[64:67], v[146:149], v[178:181], v[64:67]
	v_mfma_f32_16x16x32_bf16 v[60:63], v[154:157], v[178:181], v[60:63]
	v_mfma_f32_16x16x32_bf16 v[48:51], v[146:149], v[186:189], v[48:51]
	v_mfma_f32_16x16x32_bf16 v[44:47], v[154:157], v[186:189], v[44:47]
	v_mfma_f32_16x16x32_bf16 v[32:35], v[146:149], v[204:207], v[32:35]
	v_mfma_f32_16x16x32_bf16 v[28:31], v[154:157], v[204:207], v[28:31]
	v_mfma_f32_16x16x32_bf16 v[16:19], v[146:149], v[212:215], v[16:19]
	v_mfma_f32_16x16x32_bf16 v[12:15], v[154:157], v[212:215], v[12:15]
	v_mfma_f32_16x16x32_bf16 v[64:67], v[150:153], v[182:185], v[64:67]
	v_mfma_f32_16x16x32_bf16 v[60:63], v[158:161], v[182:185], v[60:63]
	v_mfma_f32_16x16x32_bf16 v[48:51], v[150:153], v[190:193], v[48:51]
	v_mfma_f32_16x16x32_bf16 v[44:47], v[158:161], v[190:193], v[44:47]
	v_mfma_f32_16x16x32_bf16 v[32:35], v[150:153], v[208:211], v[32:35]
	v_mfma_f32_16x16x32_bf16 v[28:31], v[158:161], v[208:211], v[28:31]
	v_mfma_f32_16x16x32_bf16 v[16:19], v[150:153], v[226:229], v[16:19]
	v_mfma_f32_16x16x32_bf16 v[12:15], v[158:161], v[226:229], v[12:15]
	s_setprio 0
	s_setprio 1
	v_mfma_f32_16x16x32_bf16 v[56:59], v[162:165], v[178:181], v[56:59]
	v_mfma_f32_16x16x32_bf16 v[52:55], v[170:173], v[178:181], v[52:55]
	v_mfma_f32_16x16x32_bf16 v[40:43], v[162:165], v[186:189], v[40:43]
	v_mfma_f32_16x16x32_bf16 v[36:39], v[170:173], v[186:189], v[36:39]
	v_mfma_f32_16x16x32_bf16 v[24:27], v[162:165], v[204:207], v[24:27]
	v_mfma_f32_16x16x32_bf16 v[20:23], v[170:173], v[204:207], v[20:23]
	v_mfma_f32_16x16x32_bf16 v[8:11], v[162:165], v[212:215], v[8:11]
	v_mfma_f32_16x16x32_bf16 v[4:7], v[170:173], v[212:215], v[4:7]
	v_mfma_f32_16x16x32_bf16 v[56:59], v[166:169], v[182:185], v[56:59]
	v_mfma_f32_16x16x32_bf16 v[52:55], v[174:177], v[182:185], v[52:55]
	v_mfma_f32_16x16x32_bf16 v[40:43], v[166:169], v[190:193], v[40:43]
	v_mfma_f32_16x16x32_bf16 v[36:39], v[174:177], v[190:193], v[36:39]
	v_mfma_f32_16x16x32_bf16 v[24:27], v[166:169], v[208:211], v[24:27]
	v_mfma_f32_16x16x32_bf16 v[20:23], v[174:177], v[208:211], v[20:23]
	v_mfma_f32_16x16x32_bf16 v[8:11], v[166:169], v[226:229], v[8:11]
	v_mfma_f32_16x16x32_bf16 v[4:7], v[174:177], v[226:229], v[4:7]
	s_setprio 0
	s_barrier
	s_add_i32 s58, 0, 0x18000
	s_add_i32 s59, 0, 0x1c000
	s_add_u32 s22, s22, 0x80000
	s_addc_u32 s23, s23, 0
	s_mov_b32 m0, s37
	v_lshl_add_u64 v[236:237], s[22:23], 0, v[136:137]
	global_load_lds_dwordx4 v[236:237], off
	v_lshl_add_u64 v[236:237], s[22:23], 0, v[140:141]
	s_mov_b32 m0, s38
	s_nop 0
	global_load_lds_dwordx4 v[236:237], off
	v_add_u32_e32 v2, s58, v1
	ds_read_b128 v[146:149], v2
	ds_read_b128 v[150:153], v2 offset:1024
	ds_read_b128 v[154:157], v2 offset:2048
	ds_read_b128 v[158:161], v2 offset:3072
	v_add_u32_e32 v2, s59, v1
	ds_read_b128 v[162:165], v2
	ds_read_b128 v[166:169], v2 offset:1024
	ds_read_b128 v[170:173], v2 offset:2048
	ds_read_b128 v[174:177], v2 offset:3072
	ds_read_b128 v[178:181], v133 offset:32768
	ds_read_b128 v[182:185], v133 offset:33792
	ds_read_b128 v[186:189], v133 offset:34816
	ds_read_b128 v[190:193], v133 offset:35840
	ds_read_b128 v[204:207], v133 offset:36864
	ds_read_b128 v[208:211], v133 offset:37888
	ds_read_b128 v[212:215], v133 offset:38912
	ds_read_b128 v[226:229], v133 offset:39936
	s_waitcnt vmcnt(8)
	s_waitcnt lgkmcnt(0)
	s_barrier
	s_setprio 1
	s_waitcnt lgkmcnt(0)
	v_mfma_f32_16x16x32_bf16 v[128:131], v[146:149], v[178:181], v[128:131]
	v_mfma_f32_16x16x32_bf16 v[124:127], v[154:157], v[178:181], v[124:127]
	v_mfma_f32_16x16x32_bf16 v[112:115], v[146:149], v[186:189], v[112:115]
	v_mfma_f32_16x16x32_bf16 v[108:111], v[154:157], v[186:189], v[108:111]
	v_mfma_f32_16x16x32_bf16 v[96:99], v[146:149], v[204:207], v[96:99]
	v_mfma_f32_16x16x32_bf16 v[92:95], v[154:157], v[204:207], v[92:95]
	v_mfma_f32_16x16x32_bf16 v[80:83], v[146:149], v[212:215], v[80:83]
	v_mfma_f32_16x16x32_bf16 v[76:79], v[154:157], v[212:215], v[76:79]
	v_mfma_f32_16x16x32_bf16 v[128:131], v[150:153], v[182:185], v[128:131]
	v_mfma_f32_16x16x32_bf16 v[124:127], v[158:161], v[182:185], v[124:127]
	v_mfma_f32_16x16x32_bf16 v[112:115], v[150:153], v[190:193], v[112:115]
	v_mfma_f32_16x16x32_bf16 v[108:111], v[158:161], v[190:193], v[108:111]
	v_mfma_f32_16x16x32_bf16 v[96:99], v[150:153], v[208:211], v[96:99]
	v_mfma_f32_16x16x32_bf16 v[92:95], v[158:161], v[208:211], v[92:95]
	v_mfma_f32_16x16x32_bf16 v[80:83], v[150:153], v[226:229], v[80:83]
	v_mfma_f32_16x16x32_bf16 v[76:79], v[158:161], v[226:229], v[76:79]
	s_setprio 0
	s_setprio 1
	v_mfma_f32_16x16x32_bf16 v[120:123], v[162:165], v[178:181], v[120:123]
	v_mfma_f32_16x16x32_bf16 v[116:119], v[170:173], v[178:181], v[116:119]
	v_mfma_f32_16x16x32_bf16 v[104:107], v[162:165], v[186:189], v[104:107]
	v_mfma_f32_16x16x32_bf16 v[100:103], v[170:173], v[186:189], v[100:103]
	v_mfma_f32_16x16x32_bf16 v[88:91], v[162:165], v[204:207], v[88:91]
	v_mfma_f32_16x16x32_bf16 v[84:87], v[170:173], v[204:207], v[84:87]
	v_mfma_f32_16x16x32_bf16 v[72:75], v[162:165], v[212:215], v[72:75]
	v_mfma_f32_16x16x32_bf16 v[68:71], v[170:173], v[212:215], v[68:71]
	v_mfma_f32_16x16x32_bf16 v[120:123], v[166:169], v[182:185], v[120:123]
	v_mfma_f32_16x16x32_bf16 v[116:119], v[174:177], v[182:185], v[116:119]
	v_mfma_f32_16x16x32_bf16 v[104:107], v[166:169], v[190:193], v[104:107]
	v_mfma_f32_16x16x32_bf16 v[100:103], v[174:177], v[190:193], v[100:103]
	v_mfma_f32_16x16x32_bf16 v[88:91], v[166:169], v[208:211], v[88:91]
	v_mfma_f32_16x16x32_bf16 v[84:87], v[174:177], v[208:211], v[84:87]
	v_mfma_f32_16x16x32_bf16 v[72:75], v[166:169], v[226:229], v[72:75]
	v_mfma_f32_16x16x32_bf16 v[68:71], v[174:177], v[226:229], v[68:71]
	s_setprio 0
	s_barrier
	s_add_i32 s22, s58, s34
	v_lshl_add_u64 v[194:195], v[194:195], 0, s[94:95]
	s_mov_b32 m0, s22
	s_nop 0
	global_load_lds_dwordx4 v[194:195], off
	s_add_i32 m0, s22, 0x2000
	s_add_u32 s20, s20, 0x80080
	v_lshl_add_u64 v[194:195], v[230:231], 0, s[94:95]
	s_addc_u32 s21, s21, 0
	s_add_i32 s22, s59, s34
	global_load_lds_dwordx4 v[194:195], off
	v_lshl_add_u64 v[194:195], s[20:21], 0, v[134:135]
	s_mov_b32 m0, s22
	s_nop 0
	global_load_lds_dwordx4 v[194:195], off
	v_lshl_add_u64 v[194:195], s[20:21], 0, v[138:139]
	s_add_i32 m0, s22, 0x2000
	s_nop 0
	global_load_lds_dwordx4 v[194:195], off
	v_lshl_add_u64 v[194:195], v[232:233], 0, s[94:95]
	s_mov_b32 m0, s41
	s_nop 0
	global_load_lds_dwordx4 v[194:195], off
	v_lshl_add_u64 v[194:195], v[234:235], 0, s[94:95]
	s_mov_b32 m0, s42
	s_nop 0
	global_load_lds_dwordx4 v[194:195], off
	ds_read_b128 v[178:181], v133 offset:49152
	ds_read_b128 v[182:185], v133 offset:50176
	ds_read_b128 v[186:189], v133 offset:51200
	ds_read_b128 v[190:193], v133 offset:52224
	ds_read_b128 v[204:207], v133 offset:53248
	ds_read_b128 v[208:211], v133 offset:54272
	ds_read_b128 v[212:215], v133 offset:55296
	ds_read_b128 v[226:229], v133 offset:56320
	s_waitcnt vmcnt(8)
	s_waitcnt lgkmcnt(0)
	s_barrier
	s_setprio 1
	s_waitcnt lgkmcnt(0)
	v_mfma_f32_16x16x32_bf16 v[64:67], v[146:149], v[178:181], v[64:67]
	v_mfma_f32_16x16x32_bf16 v[60:63], v[154:157], v[178:181], v[60:63]
	v_mfma_f32_16x16x32_bf16 v[48:51], v[146:149], v[186:189], v[48:51]
	v_mfma_f32_16x16x32_bf16 v[44:47], v[154:157], v[186:189], v[44:47]
	v_mfma_f32_16x16x32_bf16 v[32:35], v[146:149], v[204:207], v[32:35]
	v_mfma_f32_16x16x32_bf16 v[28:31], v[154:157], v[204:207], v[28:31]
	v_mfma_f32_16x16x32_bf16 v[16:19], v[146:149], v[212:215], v[16:19]
	v_mfma_f32_16x16x32_bf16 v[12:15], v[154:157], v[212:215], v[12:15]
	v_mfma_f32_16x16x32_bf16 v[64:67], v[150:153], v[182:185], v[64:67]
	v_mfma_f32_16x16x32_bf16 v[60:63], v[158:161], v[182:185], v[60:63]
	v_mfma_f32_16x16x32_bf16 v[48:51], v[150:153], v[190:193], v[48:51]
	v_mfma_f32_16x16x32_bf16 v[44:47], v[158:161], v[190:193], v[44:47]
	v_mfma_f32_16x16x32_bf16 v[32:35], v[150:153], v[208:211], v[32:35]
	v_mfma_f32_16x16x32_bf16 v[28:31], v[158:161], v[208:211], v[28:31]
	v_mfma_f32_16x16x32_bf16 v[16:19], v[150:153], v[226:229], v[16:19]
	v_mfma_f32_16x16x32_bf16 v[12:15], v[158:161], v[226:229], v[12:15]
	s_setprio 0
	s_setprio 1
	v_mfma_f32_16x16x32_bf16 v[56:59], v[162:165], v[178:181], v[56:59]
	v_mfma_f32_16x16x32_bf16 v[52:55], v[170:173], v[178:181], v[52:55]
	v_mfma_f32_16x16x32_bf16 v[40:43], v[162:165], v[186:189], v[40:43]
	v_mfma_f32_16x16x32_bf16 v[36:39], v[170:173], v[186:189], v[36:39]
	v_mfma_f32_16x16x32_bf16 v[24:27], v[162:165], v[204:207], v[24:27]
	v_mfma_f32_16x16x32_bf16 v[20:23], v[170:173], v[204:207], v[20:23]
	v_mfma_f32_16x16x32_bf16 v[8:11], v[162:165], v[212:215], v[8:11]
	v_mfma_f32_16x16x32_bf16 v[4:7], v[170:173], v[212:215], v[4:7]
	v_mfma_f32_16x16x32_bf16 v[56:59], v[166:169], v[182:185], v[56:59]
	v_mfma_f32_16x16x32_bf16 v[52:55], v[174:177], v[182:185], v[52:55]
	v_mfma_f32_16x16x32_bf16 v[40:43], v[166:169], v[190:193], v[40:43]
	v_mfma_f32_16x16x32_bf16 v[36:39], v[174:177], v[190:193], v[36:39]
	v_mfma_f32_16x16x32_bf16 v[24:27], v[166:169], v[208:211], v[24:27]
	v_mfma_f32_16x16x32_bf16 v[20:23], v[174:177], v[208:211], v[20:23]
	v_mfma_f32_16x16x32_bf16 v[8:11], v[166:169], v[226:229], v[8:11]
	v_mfma_f32_16x16x32_bf16 v[4:7], v[174:177], v[226:229], v[4:7]
	s_setprio 0
	s_barrier
	s_add_i32 s49, s49, 2
	s_add_u32 s3, s3, 0x100
	s_addc_u32 s46, s46, 0
	s_add_u32 s18, s18, 0x100
	s_addc_u32 s19, s19, 0
	s_cmp_gt_u32 s49, 29
	s_cbranch_scc0 .LBB0_236
	s_and_b64 vcc, exec, s[10:11]
	s_cbranch_vccz .LBB0_239
	s_barrier

.LBB0_724:
	s_add_u32 s18, s16, 0xfff80080
	s_addc_u32 s19, s17, -1
	s_add_i32 s44, 0, 0x10000
	s_cmp_eq_u32 s43, 28
	s_cselect_b32 s21, s13, s19
	s_cselect_b32 s20, s12, s18
	s_cselect_b32 s19, s15, s42
	s_cselect_b32 s18, s14, s7
	s_add_i32 s46, 0, 0x14000
	v_lshl_add_u64 v[194:195], s[16:17], 0, v[142:143]
	s_add_i32 m0, s28, 0xc000
	s_nop 0
	global_load_lds_dwordx4 v[194:195], off
	v_lshl_add_u64 v[194:195], s[16:17], 0, v[140:141]
	s_add_i32 m0, s28, 0xe000
	s_nop 0
	global_load_lds_dwordx4 v[194:195], off
	v_add_u32_e32 v2, s44, v1
	ds_read_b128 v[146:149], v2
	ds_read_b128 v[150:153], v2 offset:1024
	ds_read_b128 v[154:157], v2 offset:2048
	ds_read_b128 v[158:161], v2 offset:3072
	v_add_u32_e32 v2, s46, v1
	ds_read_b128 v[162:165], v2
	ds_read_b128 v[166:169], v2 offset:1024
	ds_read_b128 v[170:173], v2 offset:2048
	ds_read_b128 v[174:177], v2 offset:3072
	ds_read_b128 v[178:181], v144
	ds_read_b128 v[182:185], v144 offset:1024
	ds_read_b128 v[186:189], v144 offset:2048
	ds_read_b128 v[190:193], v144 offset:3072
	ds_read_b128 v[204:207], v144 offset:4096
	ds_read_b128 v[208:211], v144 offset:5120
	ds_read_b128 v[212:215], v144 offset:6144
	ds_read_b128 v[226:229], v144 offset:7168
	s_waitcnt vmcnt(8)
	s_waitcnt lgkmcnt(0)
	s_barrier
	s_setprio 1
	s_waitcnt lgkmcnt(0)
	v_mfma_f32_16x16x32_bf16 v[128:131], v[146:149], v[178:181], v[128:131]
	v_mfma_f32_16x16x32_bf16 v[124:127], v[154:157], v[178:181], v[124:127]
	v_mfma_f32_16x16x32_bf16 v[112:115], v[146:149], v[186:189], v[112:115]
	v_mfma_f32_16x16x32_bf16 v[108:111], v[154:157], v[186:189], v[108:111]
	v_mfma_f32_16x16x32_bf16 v[96:99], v[146:149], v[204:207], v[96:99]
	v_mfma_f32_16x16x32_bf16 v[92:95], v[154:157], v[204:207], v[92:95]
	v_mfma_f32_16x16x32_bf16 v[80:83], v[146:149], v[212:215], v[80:83]
	v_mfma_f32_16x16x32_bf16 v[76:79], v[154:157], v[212:215], v[76:79]
	v_mfma_f32_16x16x32_bf16 v[128:131], v[150:153], v[182:185], v[128:131]
	v_mfma_f32_16x16x32_bf16 v[124:127], v[158:161], v[182:185], v[124:127]
	v_mfma_f32_16x16x32_bf16 v[112:115], v[150:153], v[190:193], v[112:115]
	v_mfma_f32_16x16x32_bf16 v[108:111], v[158:161], v[190:193], v[108:111]
	v_mfma_f32_16x16x32_bf16 v[96:99], v[150:153], v[208:211], v[96:99]
	v_mfma_f32_16x16x32_bf16 v[92:95], v[158:161], v[208:211], v[92:95]
	v_mfma_f32_16x16x32_bf16 v[80:83], v[150:153], v[226:229], v[80:83]
	v_mfma_f32_16x16x32_bf16 v[76:79], v[158:161], v[226:229], v[76:79]
	s_setprio 0
	s_setprio 1
	v_mfma_f32_16x16x32_bf16 v[120:123], v[162:165], v[178:181], v[120:123]
	v_mfma_f32_16x16x32_bf16 v[116:119], v[170:173], v[178:181], v[116:119]
	v_mfma_f32_16x16x32_bf16 v[104:107], v[162:165], v[186:189], v[104:107]
	v_mfma_f32_16x16x32_bf16 v[100:103], v[170:173], v[186:189], v[100:103]
	v_mfma_f32_16x16x32_bf16 v[88:91], v[162:165], v[204:207], v[88:91]
	v_mfma_f32_16x16x32_bf16 v[84:87], v[170:173], v[204:207], v[84:87]
	v_mfma_f32_16x16x32_bf16 v[72:75], v[162:165], v[212:215], v[72:75]
	v_mfma_f32_16x16x32_bf16 v[68:71], v[170:173], v[212:215], v[68:71]
	v_mfma_f32_16x16x32_bf16 v[120:123], v[166:169], v[182:185], v[120:123]
	v_mfma_f32_16x16x32_bf16 v[116:119], v[174:177], v[182:185], v[116:119]
	v_mfma_f32_16x16x32_bf16 v[104:107], v[166:169], v[190:193], v[104:107]
	v_mfma_f32_16x16x32_bf16 v[100:103], v[174:177], v[190:193], v[100:103]
	v_mfma_f32_16x16x32_bf16 v[88:91], v[166:169], v[208:211], v[88:91]
	v_mfma_f32_16x16x32_bf16 v[84:87], v[174:177], v[208:211], v[84:87]
	v_mfma_f32_16x16x32_bf16 v[72:75], v[166:169], v[226:229], v[72:75]
	v_mfma_f32_16x16x32_bf16 v[68:71], v[174:177], v[226:229], v[68:71]
	s_setprio 0
	s_barrier
	s_add_i32 s44, s44, s27
	v_lshl_add_u64 v[194:195], s[18:19], 0, v[132:133]
	s_mov_b32 m0, s44
	s_nop 0
	global_load_lds_dwordx4 v[194:195], off
	s_add_i32 m0, s44, 0x2000
	s_add_u32 s44, s18, 0x80000
	v_lshl_add_u64 v[230:231], s[18:19], 0, v[136:137]
	s_addc_u32 s45, s19, 0
	s_add_i32 s46, s46, s27
	global_load_lds_dwordx4 v[230:231], off
	v_lshl_add_u64 v[232:233], s[44:45], 0, v[132:133]
	s_mov_b32 m0, s46
	v_lshl_add_u64 v[234:235], s[20:21], 0, v[138:139]
	global_load_lds_dwordx4 v[232:233], off
	v_lshl_add_u64 v[232:233], s[44:45], 0, v[136:137]
	s_add_i32 m0, s46, 0x2000
	s_nop 0
	global_load_lds_dwordx4 v[232:233], off
	v_lshl_add_u64 v[232:233], s[20:21], 0, v[134:135]
	s_mov_b32 m0, s28
	s_nop 0
	global_load_lds_dwordx4 v[232:233], off
	s_mov_b32 m0, s29
	s_nop 0
	global_load_lds_dwordx4 v[234:235], off
	ds_read_b128 v[178:181], v144 offset:16384
	ds_read_b128 v[182:185], v144 offset:17408
	ds_read_b128 v[186:189], v144 offset:18432
	ds_read_b128 v[190:193], v144 offset:19456
	ds_read_b128 v[204:207], v144 offset:20480
	ds_read_b128 v[208:211], v144 offset:21504
	ds_read_b128 v[212:215], v144 offset:22528
	ds_read_b128 v[226:229], v144 offset:23552
	s_waitcnt vmcnt(8)
	s_waitcnt lgkmcnt(0)
	s_barrier
	s_setprio 1
	s_waitcnt lgkmcnt(0)
	v_mfma_f32_16x16x32_bf16 v[64:67], v[146:149], v[178:181], v[64:67]
	v_mfma_f32_16x16x32_bf16 v[60:63], v[154:157], v[178:181], v[60:63]
	v_mfma_f32_16x16x32_bf16 v[48:51], v[146:149], v[186:189], v[48:51]
	v_mfma_f32_16x16x32_bf16 v[44:47], v[154:157], v[186:189], v[44:47]
	v_mfma_f32_16x16x32_bf16 v[32:35], v[146:149], v[204:207], v[32:35]
	v_mfma_f32_16x16x32_bf16 v[28:31], v[154:157], v[204:207], v[28:31]
	v_mfma_f32_16x16x32_bf16 v[16:19], v[146:149], v[212:215], v[16:19]
	v_mfma_f32_16x16x32_bf16 v[12:15], v[154:157], v[212:215], v[12:15]
	v_mfma_f32_16x16x32_bf16 v[64:67], v[150:153], v[182:185], v[64:67]
	v_mfma_f32_16x16x32_bf16 v[60:63], v[158:161], v[182:185], v[60:63]
	v_mfma_f32_16x16x32_bf16 v[48:51], v[150:153], v[190:193], v[48:51]
	v_mfma_f32_16x16x32_bf16 v[44:47], v[158:161], v[190:193], v[44:47]
	v_mfma_f32_16x16x32_bf16 v[32:35], v[150:153], v[208:211], v[32:35]
	v_mfma_f32_16x16x32_bf16 v[28:31], v[158:161], v[208:211], v[28:31]
	v_mfma_f32_16x16x32_bf16 v[16:19], v[150:153], v[226:229], v[16:19]
	v_mfma_f32_16x16x32_bf16 v[12:15], v[158:161], v[226:229], v[12:15]
	s_setprio 0
	s_setprio 1
	v_mfma_f32_16x16x32_bf16 v[56:59], v[162:165], v[178:181], v[56:59]
	v_mfma_f32_16x16x32_bf16 v[52:55], v[170:173], v[178:181], v[52:55]
	v_mfma_f32_16x16x32_bf16 v[40:43], v[162:165], v[186:189], v[40:43]
	v_mfma_f32_16x16x32_bf16 v[36:39], v[170:173], v[186:189], v[36:39]
	v_mfma_f32_16x16x32_bf16 v[24:27], v[162:165], v[204:207], v[24:27]
	v_mfma_f32_16x16x32_bf16 v[20:23], v[170:173], v[204:207], v[20:23]
	v_mfma_f32_16x16x32_bf16 v[8:11], v[162:165], v[212:215], v[8:11]
	v_mfma_f32_16x16x32_bf16 v[4:7], v[170:173], v[212:215], v[4:7]
	v_mfma_f32_16x16x32_bf16 v[56:59], v[166:169], v[182:185], v[56:59]
	v_mfma_f32_16x16x32_bf16 v[52:55], v[174:177], v[182:185], v[52:55]
	v_mfma_f32_16x16x32_bf16 v[40:43], v[166:169], v[190:193], v[40:43]
	v_mfma_f32_16x16x32_bf16 v[36:39], v[174:177], v[190:193], v[36:39]
	v_mfma_f32_16x16x32_bf16 v[24:27], v[166:169], v[208:211], v[24:27]
	v_mfma_f32_16x16x32_bf16 v[20:23], v[174:177], v[208:211], v[20:23]
	v_mfma_f32_16x16x32_bf16 v[8:11], v[166:169], v[226:229], v[8:11]
	v_mfma_f32_16x16x32_bf16 v[4:7], v[174:177], v[226:229], v[4:7]
	s_setprio 0
	s_barrier
	s_add_i32 s44, 0, 0x18000
	s_add_i32 s45, 0, 0x1c000
	s_add_u32 s20, s20, 0x80000
	s_addc_u32 s21, s21, 0
	s_mov_b32 m0, s30
	v_lshl_add_u64 v[236:237], s[20:21], 0, v[134:135]
	global_load_lds_dwordx4 v[236:237], off
	v_lshl_add_u64 v[236:237], s[20:21], 0, v[138:139]
	s_mov_b32 m0, s31
	s_nop 0
	global_load_lds_dwordx4 v[236:237], off
	v_add_u32_e32 v2, s44, v1
	ds_read_b128 v[146:149], v2
	ds_read_b128 v[150:153], v2 offset:1024
	ds_read_b128 v[154:157], v2 offset:2048
	ds_read_b128 v[158:161], v2 offset:3072
	v_add_u32_e32 v2, s45, v1
	ds_read_b128 v[162:165], v2
	ds_read_b128 v[166:169], v2 offset:1024
	ds_read_b128 v[170:173], v2 offset:2048
	ds_read_b128 v[174:177], v2 offset:3072
	ds_read_b128 v[178:181], v144 offset:32768
	ds_read_b128 v[182:185], v144 offset:33792
	ds_read_b128 v[186:189], v144 offset:34816
	ds_read_b128 v[190:193], v144 offset:35840
	ds_read_b128 v[204:207], v144 offset:36864
	ds_read_b128 v[208:211], v144 offset:37888
	ds_read_b128 v[212:215], v144 offset:38912
	ds_read_b128 v[226:229], v144 offset:39936
	s_waitcnt vmcnt(8)
	s_waitcnt lgkmcnt(0)
	s_barrier
	s_setprio 1
	s_waitcnt lgkmcnt(0)
	v_mfma_f32_16x16x32_bf16 v[128:131], v[146:149], v[178:181], v[128:131]
	v_mfma_f32_16x16x32_bf16 v[124:127], v[154:157], v[178:181], v[124:127]
	v_mfma_f32_16x16x32_bf16 v[112:115], v[146:149], v[186:189], v[112:115]
	v_mfma_f32_16x16x32_bf16 v[108:111], v[154:157], v[186:189], v[108:111]
	v_mfma_f32_16x16x32_bf16 v[96:99], v[146:149], v[204:207], v[96:99]
	v_mfma_f32_16x16x32_bf16 v[92:95], v[154:157], v[204:207], v[92:95]
	v_mfma_f32_16x16x32_bf16 v[80:83], v[146:149], v[212:215], v[80:83]
	v_mfma_f32_16x16x32_bf16 v[76:79], v[154:157], v[212:215], v[76:79]
	v_mfma_f32_16x16x32_bf16 v[128:131], v[150:153], v[182:185], v[128:131]
	v_mfma_f32_16x16x32_bf16 v[124:127], v[158:161], v[182:185], v[124:127]
	v_mfma_f32_16x16x32_bf16 v[112:115], v[150:153], v[190:193], v[112:115]
	v_mfma_f32_16x16x32_bf16 v[108:111], v[158:161], v[190:193], v[108:111]
	v_mfma_f32_16x16x32_bf16 v[96:99], v[150:153], v[208:211], v[96:99]
	v_mfma_f32_16x16x32_bf16 v[92:95], v[158:161], v[208:211], v[92:95]
	v_mfma_f32_16x16x32_bf16 v[80:83], v[150:153], v[226:229], v[80:83]
	v_mfma_f32_16x16x32_bf16 v[76:79], v[158:161], v[226:229], v[76:79]
	s_setprio 0
	s_setprio 1
	v_mfma_f32_16x16x32_bf16 v[120:123], v[162:165], v[178:181], v[120:123]
	v_mfma_f32_16x16x32_bf16 v[116:119], v[170:173], v[178:181], v[116:119]
	v_mfma_f32_16x16x32_bf16 v[104:107], v[162:165], v[186:189], v[104:107]
	v_mfma_f32_16x16x32_bf16 v[100:103], v[170:173], v[186:189], v[100:103]
	v_mfma_f32_16x16x32_bf16 v[88:91], v[162:165], v[204:207], v[88:91]
	v_mfma_f32_16x16x32_bf16 v[84:87], v[170:173], v[204:207], v[84:87]
	v_mfma_f32_16x16x32_bf16 v[72:75], v[162:165], v[212:215], v[72:75]
	v_mfma_f32_16x16x32_bf16 v[68:71], v[170:173], v[212:215], v[68:71]
	v_mfma_f32_16x16x32_bf16 v[120:123], v[166:169], v[182:185], v[120:123]
	v_mfma_f32_16x16x32_bf16 v[116:119], v[174:177], v[182:185], v[116:119]
	v_mfma_f32_16x16x32_bf16 v[104:107], v[166:169], v[190:193], v[104:107]
	v_mfma_f32_16x16x32_bf16 v[100:103], v[174:177], v[190:193], v[100:103]
	v_mfma_f32_16x16x32_bf16 v[88:91], v[166:169], v[208:211], v[88:91]
	v_mfma_f32_16x16x32_bf16 v[84:87], v[174:177], v[208:211], v[84:87]
	v_mfma_f32_16x16x32_bf16 v[72:75], v[166:169], v[226:229], v[72:75]
	v_mfma_f32_16x16x32_bf16 v[68:71], v[174:177], v[226:229], v[68:71]
	s_setprio 0
	s_barrier
	s_add_i32 s20, s44, s27
	v_lshl_add_u64 v[194:195], v[194:195], 0, s[94:95]
	s_mov_b32 m0, s20
	s_nop 0
	global_load_lds_dwordx4 v[194:195], off
	s_add_i32 m0, s20, 0x2000
	s_add_u32 s18, s18, 0x80080
	v_lshl_add_u64 v[194:195], v[230:231], 0, s[94:95]
	s_addc_u32 s19, s19, 0
	s_add_i32 s20, s45, s27
	global_load_lds_dwordx4 v[194:195], off
	v_lshl_add_u64 v[194:195], s[18:19], 0, v[132:133]
	s_mov_b32 m0, s20
	s_nop 0
	global_load_lds_dwordx4 v[194:195], off
	v_lshl_add_u64 v[194:195], s[18:19], 0, v[136:137]
	s_add_i32 m0, s20, 0x2000
	s_nop 0
	global_load_lds_dwordx4 v[194:195], off
	v_lshl_add_u64 v[194:195], v[232:233], 0, s[94:95]
	s_mov_b32 m0, s36
	s_nop 0
	global_load_lds_dwordx4 v[194:195], off
	v_lshl_add_u64 v[194:195], v[234:235], 0, s[94:95]
	s_mov_b32 m0, s37
	s_nop 0
	global_load_lds_dwordx4 v[194:195], off
	ds_read_b128 v[178:181], v144 offset:49152
	ds_read_b128 v[182:185], v144 offset:50176
	ds_read_b128 v[186:189], v144 offset:51200
	ds_read_b128 v[190:193], v144 offset:52224
	ds_read_b128 v[204:207], v144 offset:53248
	ds_read_b128 v[208:211], v144 offset:54272
	ds_read_b128 v[212:215], v144 offset:55296
	ds_read_b128 v[226:229], v144 offset:56320
	s_waitcnt vmcnt(8)
	s_waitcnt lgkmcnt(0)
	s_barrier
	s_setprio 1
	s_waitcnt lgkmcnt(0)
	v_mfma_f32_16x16x32_bf16 v[64:67], v[146:149], v[178:181], v[64:67]
	v_mfma_f32_16x16x32_bf16 v[60:63], v[154:157], v[178:181], v[60:63]
	v_mfma_f32_16x16x32_bf16 v[48:51], v[146:149], v[186:189], v[48:51]
	v_mfma_f32_16x16x32_bf16 v[44:47], v[154:157], v[186:189], v[44:47]
	v_mfma_f32_16x16x32_bf16 v[32:35], v[146:149], v[204:207], v[32:35]
	v_mfma_f32_16x16x32_bf16 v[28:31], v[154:157], v[204:207], v[28:31]
	v_mfma_f32_16x16x32_bf16 v[16:19], v[146:149], v[212:215], v[16:19]
	v_mfma_f32_16x16x32_bf16 v[12:15], v[154:157], v[212:215], v[12:15]
	v_mfma_f32_16x16x32_bf16 v[64:67], v[150:153], v[182:185], v[64:67]
	v_mfma_f32_16x16x32_bf16 v[60:63], v[158:161], v[182:185], v[60:63]
	v_mfma_f32_16x16x32_bf16 v[48:51], v[150:153], v[190:193], v[48:51]
	v_mfma_f32_16x16x32_bf16 v[44:47], v[158:161], v[190:193], v[44:47]
	v_mfma_f32_16x16x32_bf16 v[32:35], v[150:153], v[208:211], v[32:35]
	v_mfma_f32_16x16x32_bf16 v[28:31], v[158:161], v[208:211], v[28:31]
	v_mfma_f32_16x16x32_bf16 v[16:19], v[150:153], v[226:229], v[16:19]
	v_mfma_f32_16x16x32_bf16 v[12:15], v[158:161], v[226:229], v[12:15]
	s_setprio 0
	s_setprio 1
	v_mfma_f32_16x16x32_bf16 v[56:59], v[162:165], v[178:181], v[56:59]
	v_mfma_f32_16x16x32_bf16 v[52:55], v[170:173], v[178:181], v[52:55]
	v_mfma_f32_16x16x32_bf16 v[40:43], v[162:165], v[186:189], v[40:43]
	v_mfma_f32_16x16x32_bf16 v[36:39], v[170:173], v[186:189], v[36:39]
	v_mfma_f32_16x16x32_bf16 v[24:27], v[162:165], v[204:207], v[24:27]
	v_mfma_f32_16x16x32_bf16 v[20:23], v[170:173], v[204:207], v[20:23]
	v_mfma_f32_16x16x32_bf16 v[8:11], v[162:165], v[212:215], v[8:11]
	v_mfma_f32_16x16x32_bf16 v[4:7], v[170:173], v[212:215], v[4:7]
	v_mfma_f32_16x16x32_bf16 v[56:59], v[166:169], v[182:185], v[56:59]
	v_mfma_f32_16x16x32_bf16 v[52:55], v[174:177], v[182:185], v[52:55]
	v_mfma_f32_16x16x32_bf16 v[40:43], v[166:169], v[190:193], v[40:43]
	v_mfma_f32_16x16x32_bf16 v[36:39], v[174:177], v[190:193], v[36:39]
	v_mfma_f32_16x16x32_bf16 v[24:27], v[166:169], v[208:211], v[24:27]
	v_mfma_f32_16x16x32_bf16 v[20:23], v[174:177], v[208:211], v[20:23]
	v_mfma_f32_16x16x32_bf16 v[8:11], v[166:169], v[226:229], v[8:11]
	v_mfma_f32_16x16x32_bf16 v[4:7], v[174:177], v[226:229], v[4:7]
	s_setprio 0
	s_barrier
	s_add_i32 s43, s43, 2
	s_add_u32 s7, s7, 0x100
	s_addc_u32 s42, s42, 0
	s_add_u32 s16, s16, 0x100
	s_addc_u32 s17, s17, 0
	s_cmp_gt_u32 s43, 29
	s_cbranch_scc0 .LBB0_724
	s_and_b64 vcc, exec, s[10:11]
	s_cbranch_vccz .LBB0_727
	s_barrier

.LBB0_909:
	s_add_u32 s22, s4, 0xfff80080
	s_addc_u32 s23, s5, -1
	s_add_i32 s55, 0, 0x10000
	s_cmp_eq_u32 s54, 28
	s_cselect_b32 s25, s19, s23
	s_cselect_b32 s24, s18, s22
	s_cselect_b32 s23, s21, s53
	s_cselect_b32 s22, s20, s52
	s_add_i32 s58, 0, 0x14000
	v_lshl_add_u64 v[160:161], s[4:5], 0, v[150:151]
	s_add_i32 m0, s35, 0xc000
	s_nop 0
	global_load_lds_dwordx4 v[160:161], off
	v_lshl_add_u64 v[160:161], s[4:5], 0, v[148:149]
	s_add_i32 m0, s35, 0xe000
	s_nop 0
	global_load_lds_dwordx4 v[160:161], off
	v_add_u32_e32 v2, s55, v1
	ds_read_b128 v[132:135], v2
	ds_read_b128 v[136:139], v2 offset:1024
	ds_read_b128 v[152:155], v2 offset:2048
	ds_read_b128 v[156:159], v2 offset:3072
	v_add_u32_e32 v2, s58, v1
	ds_read_b128 v[164:167], v2
	ds_read_b128 v[168:171], v2 offset:1024
	ds_read_b128 v[172:175], v2 offset:2048
	ds_read_b128 v[176:179], v2 offset:3072
	ds_read_b128 v[180:183], v162
	ds_read_b128 v[184:187], v162 offset:1024
	ds_read_b128 v[188:191], v162 offset:2048
	ds_read_b128 v[192:195], v162 offset:3072
	ds_read_b128 v[204:207], v162 offset:4096
	ds_read_b128 v[208:211], v162 offset:5120
	ds_read_b128 v[212:215], v162 offset:6144
	ds_read_b128 v[226:229], v162 offset:7168
	s_waitcnt vmcnt(8)
	s_waitcnt lgkmcnt(0)
	s_barrier
	s_setprio 1
	s_waitcnt lgkmcnt(0)
	v_mfma_f32_16x16x32_bf16 v[128:131], v[132:135], v[180:183], v[128:131]
	v_mfma_f32_16x16x32_bf16 v[124:127], v[152:155], v[180:183], v[124:127]
	v_mfma_f32_16x16x32_bf16 v[112:115], v[132:135], v[188:191], v[112:115]
	v_mfma_f32_16x16x32_bf16 v[108:111], v[152:155], v[188:191], v[108:111]
	v_mfma_f32_16x16x32_bf16 v[96:99], v[132:135], v[204:207], v[96:99]
	v_mfma_f32_16x16x32_bf16 v[92:95], v[152:155], v[204:207], v[92:95]
	v_mfma_f32_16x16x32_bf16 v[80:83], v[132:135], v[212:215], v[80:83]
	v_mfma_f32_16x16x32_bf16 v[76:79], v[152:155], v[212:215], v[76:79]
	v_mfma_f32_16x16x32_bf16 v[128:131], v[136:139], v[184:187], v[128:131]
	v_mfma_f32_16x16x32_bf16 v[124:127], v[156:159], v[184:187], v[124:127]
	v_mfma_f32_16x16x32_bf16 v[112:115], v[136:139], v[192:195], v[112:115]
	v_mfma_f32_16x16x32_bf16 v[108:111], v[156:159], v[192:195], v[108:111]
	v_mfma_f32_16x16x32_bf16 v[96:99], v[136:139], v[208:211], v[96:99]
	v_mfma_f32_16x16x32_bf16 v[92:95], v[156:159], v[208:211], v[92:95]
	v_mfma_f32_16x16x32_bf16 v[80:83], v[136:139], v[226:229], v[80:83]
	v_mfma_f32_16x16x32_bf16 v[76:79], v[156:159], v[226:229], v[76:79]
	s_setprio 0
	s_setprio 1
	v_mfma_f32_16x16x32_bf16 v[120:123], v[164:167], v[180:183], v[120:123]
	v_mfma_f32_16x16x32_bf16 v[116:119], v[172:175], v[180:183], v[116:119]
	v_mfma_f32_16x16x32_bf16 v[104:107], v[164:167], v[188:191], v[104:107]
	v_mfma_f32_16x16x32_bf16 v[100:103], v[172:175], v[188:191], v[100:103]
	v_mfma_f32_16x16x32_bf16 v[88:91], v[164:167], v[204:207], v[88:91]
	v_mfma_f32_16x16x32_bf16 v[84:87], v[172:175], v[204:207], v[84:87]
	v_mfma_f32_16x16x32_bf16 v[72:75], v[164:167], v[212:215], v[72:75]
	v_mfma_f32_16x16x32_bf16 v[68:71], v[172:175], v[212:215], v[68:71]
	v_mfma_f32_16x16x32_bf16 v[120:123], v[168:171], v[184:187], v[120:123]
	v_mfma_f32_16x16x32_bf16 v[116:119], v[176:179], v[184:187], v[116:119]
	v_mfma_f32_16x16x32_bf16 v[104:107], v[168:171], v[192:195], v[104:107]
	v_mfma_f32_16x16x32_bf16 v[100:103], v[176:179], v[192:195], v[100:103]
	v_mfma_f32_16x16x32_bf16 v[88:91], v[168:171], v[208:211], v[88:91]
	v_mfma_f32_16x16x32_bf16 v[84:87], v[176:179], v[208:211], v[84:87]
	v_mfma_f32_16x16x32_bf16 v[72:75], v[168:171], v[226:229], v[72:75]
	v_mfma_f32_16x16x32_bf16 v[68:71], v[176:179], v[226:229], v[68:71]
	s_setprio 0
	s_barrier
	s_add_i32 s55, s55, s34
	v_lshl_add_u64 v[160:161], s[22:23], 0, v[140:141]
	s_mov_b32 m0, s55
	s_nop 0
	global_load_lds_dwordx4 v[160:161], off
	s_add_i32 m0, s55, 0x2000
	s_add_u32 s56, s22, 0x80000
	v_lshl_add_u64 v[230:231], s[22:23], 0, v[144:145]
	s_addc_u32 s57, s23, 0
	s_add_i32 s55, s58, s34
	global_load_lds_dwordx4 v[230:231], off
	v_lshl_add_u64 v[232:233], s[56:57], 0, v[140:141]
	s_mov_b32 m0, s55
	v_lshl_add_u64 v[234:235], s[24:25], 0, v[146:147]
	global_load_lds_dwordx4 v[232:233], off
	v_lshl_add_u64 v[232:233], s[56:57], 0, v[144:145]
	s_add_i32 m0, s55, 0x2000
	s_nop 0
	global_load_lds_dwordx4 v[232:233], off
	v_lshl_add_u64 v[232:233], s[24:25], 0, v[142:143]
	s_mov_b32 m0, s35
	s_nop 0
	global_load_lds_dwordx4 v[232:233], off
	s_mov_b32 m0, s36
	s_nop 0
	global_load_lds_dwordx4 v[234:235], off
	ds_read_b128 v[180:183], v162 offset:16384
	ds_read_b128 v[184:187], v162 offset:17408
	ds_read_b128 v[188:191], v162 offset:18432
	ds_read_b128 v[192:195], v162 offset:19456
	ds_read_b128 v[204:207], v162 offset:20480
	ds_read_b128 v[208:211], v162 offset:21504
	ds_read_b128 v[212:215], v162 offset:22528
	ds_read_b128 v[226:229], v162 offset:23552
	s_waitcnt vmcnt(8)
	s_waitcnt lgkmcnt(0)
	s_barrier
	s_setprio 1
	s_waitcnt lgkmcnt(0)
	v_mfma_f32_16x16x32_bf16 v[64:67], v[132:135], v[180:183], v[64:67]
	v_mfma_f32_16x16x32_bf16 v[60:63], v[152:155], v[180:183], v[60:63]
	v_mfma_f32_16x16x32_bf16 v[48:51], v[132:135], v[188:191], v[48:51]
	v_mfma_f32_16x16x32_bf16 v[44:47], v[152:155], v[188:191], v[44:47]
	v_mfma_f32_16x16x32_bf16 v[32:35], v[132:135], v[204:207], v[32:35]
	v_mfma_f32_16x16x32_bf16 v[28:31], v[152:155], v[204:207], v[28:31]
	v_mfma_f32_16x16x32_bf16 v[16:19], v[132:135], v[212:215], v[16:19]
	v_mfma_f32_16x16x32_bf16 v[12:15], v[152:155], v[212:215], v[12:15]
	v_mfma_f32_16x16x32_bf16 v[64:67], v[136:139], v[184:187], v[64:67]
	v_mfma_f32_16x16x32_bf16 v[60:63], v[156:159], v[184:187], v[60:63]
	v_mfma_f32_16x16x32_bf16 v[48:51], v[136:139], v[192:195], v[48:51]
	v_mfma_f32_16x16x32_bf16 v[44:47], v[156:159], v[192:195], v[44:47]
	v_mfma_f32_16x16x32_bf16 v[32:35], v[136:139], v[208:211], v[32:35]
	v_mfma_f32_16x16x32_bf16 v[28:31], v[156:159], v[208:211], v[28:31]
	v_mfma_f32_16x16x32_bf16 v[16:19], v[136:139], v[226:229], v[16:19]
	v_mfma_f32_16x16x32_bf16 v[12:15], v[156:159], v[226:229], v[12:15]
	s_setprio 0
	s_setprio 1
	v_mfma_f32_16x16x32_bf16 v[56:59], v[164:167], v[180:183], v[56:59]
	v_mfma_f32_16x16x32_bf16 v[52:55], v[172:175], v[180:183], v[52:55]
	v_mfma_f32_16x16x32_bf16 v[40:43], v[164:167], v[188:191], v[40:43]
	v_mfma_f32_16x16x32_bf16 v[36:39], v[172:175], v[188:191], v[36:39]
	v_mfma_f32_16x16x32_bf16 v[24:27], v[164:167], v[204:207], v[24:27]
	v_mfma_f32_16x16x32_bf16 v[20:23], v[172:175], v[204:207], v[20:23]
	v_mfma_f32_16x16x32_bf16 v[8:11], v[164:167], v[212:215], v[8:11]
	v_mfma_f32_16x16x32_bf16 v[4:7], v[172:175], v[212:215], v[4:7]
	v_mfma_f32_16x16x32_bf16 v[56:59], v[168:171], v[184:187], v[56:59]
	v_mfma_f32_16x16x32_bf16 v[52:55], v[176:179], v[184:187], v[52:55]
	v_mfma_f32_16x16x32_bf16 v[40:43], v[168:171], v[192:195], v[40:43]
	v_mfma_f32_16x16x32_bf16 v[36:39], v[176:179], v[192:195], v[36:39]
	v_mfma_f32_16x16x32_bf16 v[24:27], v[168:171], v[208:211], v[24:27]
	v_mfma_f32_16x16x32_bf16 v[20:23], v[176:179], v[208:211], v[20:23]
	v_mfma_f32_16x16x32_bf16 v[8:11], v[168:171], v[226:229], v[8:11]
	v_mfma_f32_16x16x32_bf16 v[4:7], v[176:179], v[226:229], v[4:7]
	s_setprio 0
	s_barrier
	s_add_i32 s55, 0, 0x18000
	s_add_i32 s56, 0, 0x1c000
	s_add_u32 s24, s24, 0x80000
	s_addc_u32 s25, s25, 0
	s_mov_b32 m0, s37
	v_lshl_add_u64 v[236:237], s[24:25], 0, v[142:143]
	global_load_lds_dwordx4 v[236:237], off
	v_lshl_add_u64 v[236:237], s[24:25], 0, v[146:147]
	s_mov_b32 m0, s38
	s_nop 0
	global_load_lds_dwordx4 v[236:237], off
	v_add_u32_e32 v2, s55, v1
	ds_read_b128 v[132:135], v2
	ds_read_b128 v[136:139], v2 offset:1024
	ds_read_b128 v[152:155], v2 offset:2048
	ds_read_b128 v[156:159], v2 offset:3072
	v_add_u32_e32 v2, s56, v1
	ds_read_b128 v[164:167], v2
	ds_read_b128 v[168:171], v2 offset:1024
	ds_read_b128 v[172:175], v2 offset:2048
	ds_read_b128 v[176:179], v2 offset:3072
	ds_read_b128 v[180:183], v162 offset:32768
	ds_read_b128 v[184:187], v162 offset:33792
	ds_read_b128 v[188:191], v162 offset:34816
	ds_read_b128 v[192:195], v162 offset:35840
	ds_read_b128 v[204:207], v162 offset:36864
	ds_read_b128 v[208:211], v162 offset:37888
	ds_read_b128 v[212:215], v162 offset:38912
	ds_read_b128 v[226:229], v162 offset:39936
	s_waitcnt vmcnt(8)
	s_waitcnt lgkmcnt(0)
	s_barrier
	s_setprio 1
	s_waitcnt lgkmcnt(0)
	v_mfma_f32_16x16x32_bf16 v[128:131], v[132:135], v[180:183], v[128:131]
	v_mfma_f32_16x16x32_bf16 v[124:127], v[152:155], v[180:183], v[124:127]
	v_mfma_f32_16x16x32_bf16 v[112:115], v[132:135], v[188:191], v[112:115]
	v_mfma_f32_16x16x32_bf16 v[108:111], v[152:155], v[188:191], v[108:111]
	v_mfma_f32_16x16x32_bf16 v[96:99], v[132:135], v[204:207], v[96:99]
	v_mfma_f32_16x16x32_bf16 v[92:95], v[152:155], v[204:207], v[92:95]
	v_mfma_f32_16x16x32_bf16 v[80:83], v[132:135], v[212:215], v[80:83]
	v_mfma_f32_16x16x32_bf16 v[76:79], v[152:155], v[212:215], v[76:79]
	v_mfma_f32_16x16x32_bf16 v[128:131], v[136:139], v[184:187], v[128:131]
	v_mfma_f32_16x16x32_bf16 v[124:127], v[156:159], v[184:187], v[124:127]
	v_mfma_f32_16x16x32_bf16 v[112:115], v[136:139], v[192:195], v[112:115]
	v_mfma_f32_16x16x32_bf16 v[108:111], v[156:159], v[192:195], v[108:111]
	v_mfma_f32_16x16x32_bf16 v[96:99], v[136:139], v[208:211], v[96:99]
	v_mfma_f32_16x16x32_bf16 v[92:95], v[156:159], v[208:211], v[92:95]
	v_mfma_f32_16x16x32_bf16 v[80:83], v[136:139], v[226:229], v[80:83]
	v_mfma_f32_16x16x32_bf16 v[76:79], v[156:159], v[226:229], v[76:79]
	s_setprio 0
	s_setprio 1
	v_mfma_f32_16x16x32_bf16 v[120:123], v[164:167], v[180:183], v[120:123]
	v_mfma_f32_16x16x32_bf16 v[116:119], v[172:175], v[180:183], v[116:119]
	v_mfma_f32_16x16x32_bf16 v[104:107], v[164:167], v[188:191], v[104:107]
	v_mfma_f32_16x16x32_bf16 v[100:103], v[172:175], v[188:191], v[100:103]
	v_mfma_f32_16x16x32_bf16 v[88:91], v[164:167], v[204:207], v[88:91]
	v_mfma_f32_16x16x32_bf16 v[84:87], v[172:175], v[204:207], v[84:87]
	v_mfma_f32_16x16x32_bf16 v[72:75], v[164:167], v[212:215], v[72:75]
	v_mfma_f32_16x16x32_bf16 v[68:71], v[172:175], v[212:215], v[68:71]
	v_mfma_f32_16x16x32_bf16 v[120:123], v[168:171], v[184:187], v[120:123]
	v_mfma_f32_16x16x32_bf16 v[116:119], v[176:179], v[184:187], v[116:119]
	v_mfma_f32_16x16x32_bf16 v[104:107], v[168:171], v[192:195], v[104:107]
	v_mfma_f32_16x16x32_bf16 v[100:103], v[176:179], v[192:195], v[100:103]
	v_mfma_f32_16x16x32_bf16 v[88:91], v[168:171], v[208:211], v[88:91]
	v_mfma_f32_16x16x32_bf16 v[84:87], v[176:179], v[208:211], v[84:87]
	v_mfma_f32_16x16x32_bf16 v[72:75], v[168:171], v[226:229], v[72:75]
	v_mfma_f32_16x16x32_bf16 v[68:71], v[176:179], v[226:229], v[68:71]
	s_setprio 0
	s_barrier
	s_add_i32 s24, s55, s34
	v_lshl_add_u64 v[160:161], v[160:161], 0, s[94:95]
	s_mov_b32 m0, s24
	s_nop 0
	global_load_lds_dwordx4 v[160:161], off
	s_add_i32 m0, s24, 0x2000
	s_add_u32 s22, s22, 0x80080
	v_lshl_add_u64 v[160:161], v[230:231], 0, s[94:95]
	s_addc_u32 s23, s23, 0
	s_add_i32 s24, s56, s34
	global_load_lds_dwordx4 v[160:161], off
	v_lshl_add_u64 v[160:161], s[22:23], 0, v[140:141]
	s_mov_b32 m0, s24
	s_nop 0
	global_load_lds_dwordx4 v[160:161], off
	v_lshl_add_u64 v[160:161], s[22:23], 0, v[144:145]
	s_add_i32 m0, s24, 0x2000
	s_nop 0
	global_load_lds_dwordx4 v[160:161], off
	v_lshl_add_u64 v[160:161], v[232:233], 0, s[94:95]
	s_mov_b32 m0, s42
	s_nop 0
	global_load_lds_dwordx4 v[160:161], off
	v_lshl_add_u64 v[160:161], v[234:235], 0, s[94:95]
	s_mov_b32 m0, s43
	s_nop 0
	global_load_lds_dwordx4 v[160:161], off
	ds_read_b128 v[180:183], v162 offset:49152
	ds_read_b128 v[184:187], v162 offset:50176
	ds_read_b128 v[188:191], v162 offset:51200
	ds_read_b128 v[192:195], v162 offset:52224
	ds_read_b128 v[204:207], v162 offset:53248
	ds_read_b128 v[208:211], v162 offset:54272
	ds_read_b128 v[212:215], v162 offset:55296
	ds_read_b128 v[226:229], v162 offset:56320
	s_waitcnt vmcnt(8)
	s_waitcnt lgkmcnt(0)
	s_barrier
	s_setprio 1
	s_waitcnt lgkmcnt(0)
	v_mfma_f32_16x16x32_bf16 v[64:67], v[132:135], v[180:183], v[64:67]
	v_mfma_f32_16x16x32_bf16 v[60:63], v[152:155], v[180:183], v[60:63]
	v_mfma_f32_16x16x32_bf16 v[48:51], v[132:135], v[188:191], v[48:51]
	v_mfma_f32_16x16x32_bf16 v[44:47], v[152:155], v[188:191], v[44:47]
	v_mfma_f32_16x16x32_bf16 v[32:35], v[132:135], v[204:207], v[32:35]
	v_mfma_f32_16x16x32_bf16 v[28:31], v[152:155], v[204:207], v[28:31]
	v_mfma_f32_16x16x32_bf16 v[16:19], v[132:135], v[212:215], v[16:19]
	v_mfma_f32_16x16x32_bf16 v[12:15], v[152:155], v[212:215], v[12:15]
	v_mfma_f32_16x16x32_bf16 v[64:67], v[136:139], v[184:187], v[64:67]
	v_mfma_f32_16x16x32_bf16 v[60:63], v[156:159], v[184:187], v[60:63]
	v_mfma_f32_16x16x32_bf16 v[48:51], v[136:139], v[192:195], v[48:51]
	v_mfma_f32_16x16x32_bf16 v[44:47], v[156:159], v[192:195], v[44:47]
	v_mfma_f32_16x16x32_bf16 v[32:35], v[136:139], v[208:211], v[32:35]
	v_mfma_f32_16x16x32_bf16 v[28:31], v[156:159], v[208:211], v[28:31]
	v_mfma_f32_16x16x32_bf16 v[16:19], v[136:139], v[226:229], v[16:19]
	v_mfma_f32_16x16x32_bf16 v[12:15], v[156:159], v[226:229], v[12:15]
	s_setprio 0
	s_setprio 1
	v_mfma_f32_16x16x32_bf16 v[56:59], v[164:167], v[180:183], v[56:59]
	v_mfma_f32_16x16x32_bf16 v[52:55], v[172:175], v[180:183], v[52:55]
	v_mfma_f32_16x16x32_bf16 v[40:43], v[164:167], v[188:191], v[40:43]
	v_mfma_f32_16x16x32_bf16 v[36:39], v[172:175], v[188:191], v[36:39]
	v_mfma_f32_16x16x32_bf16 v[24:27], v[164:167], v[204:207], v[24:27]
	v_mfma_f32_16x16x32_bf16 v[20:23], v[172:175], v[204:207], v[20:23]
	v_mfma_f32_16x16x32_bf16 v[8:11], v[164:167], v[212:215], v[8:11]
	v_mfma_f32_16x16x32_bf16 v[4:7], v[172:175], v[212:215], v[4:7]
	v_mfma_f32_16x16x32_bf16 v[56:59], v[168:171], v[184:187], v[56:59]
	v_mfma_f32_16x16x32_bf16 v[52:55], v[176:179], v[184:187], v[52:55]
	v_mfma_f32_16x16x32_bf16 v[40:43], v[168:171], v[192:195], v[40:43]
	v_mfma_f32_16x16x32_bf16 v[36:39], v[176:179], v[192:195], v[36:39]
	v_mfma_f32_16x16x32_bf16 v[24:27], v[168:171], v[208:211], v[24:27]
	v_mfma_f32_16x16x32_bf16 v[20:23], v[176:179], v[208:211], v[20:23]
	v_mfma_f32_16x16x32_bf16 v[8:11], v[168:171], v[226:229], v[8:11]
	v_mfma_f32_16x16x32_bf16 v[4:7], v[176:179], v[226:229], v[4:7]
	s_setprio 0
	s_barrier
	s_add_i32 s54, s54, 2
	s_add_u32 s52, s52, 0x100
	s_addc_u32 s53, s53, 0
	s_add_u32 s4, s4, 0x100
	s_addc_u32 s5, s5, 0
	s_cmp_gt_u32 s54, 29
	s_cbranch_scc0 .LBB0_909
	s_and_b64 vcc, exec, s[14:15]
	s_cbranch_vccz .LBB0_912
	s_barrier

.LBB0_2674:
	s_add_u32 s40, s26, s34
	s_addc_u32 s41, s27, s35
	s_add_u32 s38, s40, 0x100
	s_addc_u32 s39, s41, 0
	v_cndmask_b32_e64 v2, 0, 1, s[36:37]
	s_and_b64 s[36:37], s[30:31], exec
	s_cselect_b32 s37, s19, s39
	s_cselect_b32 s36, s25, s38
	s_add_u32 s34, s28, s34
	s_addc_u32 s35, s29, s35
	s_add_u32 s34, s34, 0x100
	s_addc_u32 s35, s35, 0
	s_add_i32 s73, 0, 0x10000
	s_and_b64 s[30:31], s[30:31], exec
	s_cselect_b32 s39, s46, s35
	s_cselect_b32 s38, s64, s34
	s_add_i32 s31, 0, 0x14000
	s_add_u32 s42, s40, 0x10080
	s_addc_u32 s43, s41, 0
	s_add_i32 s72, s73, s53
	s_add_i32 m0, s54, 0xc000
	s_add_i32 s76, s54, 0xe000
	s_add_i32 s69, s72, 0x2000
	v_add_u32_e32 v144, s73, v1
	s_add_u32 s40, s38, 0x10000
	ds_read_b128 v[132:135], v144
	ds_read_b128 v[148:151], v144 offset:1024
	ds_read_b128 v[152:155], v144 offset:2048
	ds_read_b128 v[156:159], v144 offset:3072
	v_add_u32_e32 v144, s31, v1
	s_addc_u32 s41, s39, 0
	s_add_i32 s71, s31, s53
	ds_read_b128 v[160:163], v144
	ds_read_b128 v[164:167], v144 offset:1024
	ds_read_b128 v[168:171], v144 offset:2048
	ds_read_b128 v[172:175], v144 offset:3072
	s_add_i32 s70, s71, 0x2000
	s_add_i32 s68, 0, 0x18000
	s_add_i32 s67, 0, 0x1c000
	s_add_u32 s34, s36, 0x10000
	s_addc_u32 s35, s37, 0
	s_add_i32 s66, s68, s53
	s_add_i32 s65, s66, 0x2000
	s_add_u32 s30, s38, 0x10080
	s_addc_u32 s31, s39, 0
	s_add_i32 s75, s67, s53
	s_add_i32 s73, s75, 0x2000
	v_cmp_ne_u32_e32 vcc, 1, v2
	v_lshl_add_u64 v[144:145], s[42:43], 0, v[138:139]
	ds_read_b128 v[176:179], v146
	ds_read_b128 v[180:183], v146 offset:1024
	ds_read_b128 v[184:187], v146 offset:2048
	ds_read_b128 v[188:191], v146 offset:3072
	ds_read_b128 v[192:195], v146 offset:4096
	ds_read_b128 v[204:207], v146 offset:5120
	ds_read_b128 v[208:211], v146 offset:6144
	ds_read_b128 v[212:215], v146 offset:7168
	global_load_lds_dwordx4 v[144:145], off
	v_lshl_add_u64 v[144:145], s[42:43], 0, v[142:143]
	s_mov_b32 m0, s76
	s_nop 0
	global_load_lds_dwordx4 v[144:145], off
	s_waitcnt vmcnt(8)
	s_waitcnt lgkmcnt(0)
	s_barrier
	s_setprio 1
	s_waitcnt lgkmcnt(0)
	v_mfma_f32_16x16x32_bf16 v[128:131], v[132:135], v[176:179], v[128:131]
	v_mfma_f32_16x16x32_bf16 v[124:127], v[152:155], v[176:179], v[124:127]
	v_mfma_f32_16x16x32_bf16 v[116:119], v[132:135], v[184:187], v[116:119]
	v_mfma_f32_16x16x32_bf16 v[108:111], v[152:155], v[184:187], v[108:111]
	v_mfma_f32_16x16x32_bf16 v[100:103], v[132:135], v[192:195], v[100:103]
	v_mfma_f32_16x16x32_bf16 v[92:95], v[152:155], v[192:195], v[92:95]
	v_mfma_f32_16x16x32_bf16 v[84:87], v[132:135], v[208:211], v[84:87]
	v_mfma_f32_16x16x32_bf16 v[76:79], v[152:155], v[208:211], v[76:79]
	v_mfma_f32_16x16x32_bf16 v[128:131], v[148:151], v[180:183], v[128:131]
	v_mfma_f32_16x16x32_bf16 v[124:127], v[156:159], v[180:183], v[124:127]
	v_mfma_f32_16x16x32_bf16 v[116:119], v[148:151], v[188:191], v[116:119]
	v_mfma_f32_16x16x32_bf16 v[108:111], v[156:159], v[188:191], v[108:111]
	v_mfma_f32_16x16x32_bf16 v[100:103], v[148:151], v[204:207], v[100:103]
	v_mfma_f32_16x16x32_bf16 v[92:95], v[156:159], v[204:207], v[92:95]
	v_mfma_f32_16x16x32_bf16 v[84:87], v[148:151], v[212:215], v[84:87]
	v_mfma_f32_16x16x32_bf16 v[76:79], v[156:159], v[212:215], v[76:79]
	s_setprio 0
	s_setprio 1
	v_mfma_f32_16x16x32_bf16 v[120:123], v[160:163], v[176:179], v[120:123]
	v_mfma_f32_16x16x32_bf16 v[112:115], v[168:171], v[176:179], v[112:115]
	v_mfma_f32_16x16x32_bf16 v[104:107], v[160:163], v[184:187], v[104:107]
	v_mfma_f32_16x16x32_bf16 v[96:99], v[168:171], v[184:187], v[96:99]
	v_mfma_f32_16x16x32_bf16 v[88:91], v[160:163], v[192:195], v[88:91]
	v_mfma_f32_16x16x32_bf16 v[80:83], v[168:171], v[192:195], v[80:83]
	v_mfma_f32_16x16x32_bf16 v[72:75], v[160:163], v[208:211], v[72:75]
	v_mfma_f32_16x16x32_bf16 v[68:71], v[168:171], v[208:211], v[68:71]
	v_mfma_f32_16x16x32_bf16 v[120:123], v[164:167], v[180:183], v[120:123]
	v_mfma_f32_16x16x32_bf16 v[112:115], v[172:175], v[180:183], v[112:115]
	v_mfma_f32_16x16x32_bf16 v[104:107], v[164:167], v[188:191], v[104:107]
	v_mfma_f32_16x16x32_bf16 v[96:99], v[172:175], v[188:191], v[96:99]
	v_mfma_f32_16x16x32_bf16 v[88:91], v[164:167], v[204:207], v[88:91]
	v_mfma_f32_16x16x32_bf16 v[80:83], v[172:175], v[204:207], v[80:83]
	v_mfma_f32_16x16x32_bf16 v[72:75], v[164:167], v[212:215], v[72:75]
	v_mfma_f32_16x16x32_bf16 v[68:71], v[172:175], v[212:215], v[68:71]
	s_setprio 0
	s_barrier
	s_mov_b32 m0, s72
	v_lshl_add_u64 v[144:145], s[38:39], 0, v[136:137]
	global_load_lds_dwordx4 v[144:145], off
	v_lshl_add_u64 v[226:227], s[38:39], 0, v[140:141]
	s_mov_b32 m0, s69
	v_lshl_add_u64 v[228:229], s[40:41], 0, v[136:137]
	global_load_lds_dwordx4 v[226:227], off
	s_mov_b32 m0, s71
	v_lshl_add_u64 v[230:231], s[36:37], 0, v[142:143]
	global_load_lds_dwordx4 v[228:229], off
	v_lshl_add_u64 v[228:229], s[40:41], 0, v[140:141]
	s_mov_b32 m0, s70
	s_nop 0
	global_load_lds_dwordx4 v[228:229], off
	v_lshl_add_u64 v[228:229], s[36:37], 0, v[138:139]
	s_mov_b32 m0, s54
	s_nop 0
	global_load_lds_dwordx4 v[228:229], off
	s_mov_b32 m0, s55
	s_nop 0
	global_load_lds_dwordx4 v[230:231], off
	ds_read_b128 v[176:179], v146 offset:16384
	ds_read_b128 v[180:183], v146 offset:17408
	ds_read_b128 v[184:187], v146 offset:18432
	ds_read_b128 v[188:191], v146 offset:19456
	ds_read_b128 v[192:195], v146 offset:20480
	ds_read_b128 v[204:207], v146 offset:21504
	ds_read_b128 v[208:211], v146 offset:22528
	ds_read_b128 v[212:215], v146 offset:23552
	s_waitcnt vmcnt(8)
	s_waitcnt lgkmcnt(0)
	s_barrier
	s_setprio 1
	s_waitcnt lgkmcnt(0)
	v_mfma_f32_16x16x32_bf16 v[64:67], v[132:135], v[176:179], v[64:67]
	v_mfma_f32_16x16x32_bf16 v[60:63], v[152:155], v[176:179], v[60:63]
	v_mfma_f32_16x16x32_bf16 v[52:55], v[132:135], v[184:187], v[52:55]
	v_mfma_f32_16x16x32_bf16 v[44:47], v[152:155], v[184:187], v[44:47]
	v_mfma_f32_16x16x32_bf16 v[36:39], v[132:135], v[192:195], v[36:39]
	v_mfma_f32_16x16x32_bf16 v[28:31], v[152:155], v[192:195], v[28:31]
	v_mfma_f32_16x16x32_bf16 v[20:23], v[132:135], v[208:211], v[20:23]
	v_mfma_f32_16x16x32_bf16 v[12:15], v[152:155], v[208:211], v[12:15]
	v_mfma_f32_16x16x32_bf16 v[64:67], v[148:151], v[180:183], v[64:67]
	v_mfma_f32_16x16x32_bf16 v[60:63], v[156:159], v[180:183], v[60:63]
	v_mfma_f32_16x16x32_bf16 v[52:55], v[148:151], v[188:191], v[52:55]
	v_mfma_f32_16x16x32_bf16 v[44:47], v[156:159], v[188:191], v[44:47]
	v_mfma_f32_16x16x32_bf16 v[36:39], v[148:151], v[204:207], v[36:39]
	v_mfma_f32_16x16x32_bf16 v[28:31], v[156:159], v[204:207], v[28:31]
	v_mfma_f32_16x16x32_bf16 v[20:23], v[148:151], v[212:215], v[20:23]
	v_mfma_f32_16x16x32_bf16 v[12:15], v[156:159], v[212:215], v[12:15]
	s_setprio 0
	s_setprio 1
	v_mfma_f32_16x16x32_bf16 v[56:59], v[160:163], v[176:179], v[56:59]
	v_mfma_f32_16x16x32_bf16 v[48:51], v[168:171], v[176:179], v[48:51]
	v_mfma_f32_16x16x32_bf16 v[40:43], v[160:163], v[184:187], v[40:43]
	v_mfma_f32_16x16x32_bf16 v[32:35], v[168:171], v[184:187], v[32:35]
	v_mfma_f32_16x16x32_bf16 v[24:27], v[160:163], v[192:195], v[24:27]
	v_mfma_f32_16x16x32_bf16 v[16:19], v[168:171], v[192:195], v[16:19]
	v_mfma_f32_16x16x32_bf16 v[8:11], v[160:163], v[208:211], v[8:11]
	v_mfma_f32_16x16x32_bf16 v[4:7], v[168:171], v[208:211], v[4:7]
	v_mfma_f32_16x16x32_bf16 v[56:59], v[164:167], v[180:183], v[56:59]
	v_mfma_f32_16x16x32_bf16 v[48:51], v[172:175], v[180:183], v[48:51]
	v_mfma_f32_16x16x32_bf16 v[40:43], v[164:167], v[188:191], v[40:43]
	v_mfma_f32_16x16x32_bf16 v[32:35], v[172:175], v[188:191], v[32:35]
	v_mfma_f32_16x16x32_bf16 v[24:27], v[164:167], v[204:207], v[24:27]
	v_mfma_f32_16x16x32_bf16 v[16:19], v[172:175], v[204:207], v[16:19]
	v_mfma_f32_16x16x32_bf16 v[8:11], v[164:167], v[212:215], v[8:11]
	v_mfma_f32_16x16x32_bf16 v[4:7], v[172:175], v[212:215], v[4:7]
	s_setprio 0
	s_barrier
	s_mov_b32 m0, s56
	v_lshl_add_u64 v[232:233], s[34:35], 0, v[138:139]
	global_load_lds_dwordx4 v[232:233], off
	v_lshl_add_u64 v[232:233], s[34:35], 0, v[142:143]
	s_mov_b32 m0, s57
	s_nop 0
	global_load_lds_dwordx4 v[232:233], off
	v_add_u32_e32 v2, s68, v1
	ds_read_b128 v[132:135], v2
	ds_read_b128 v[148:151], v2 offset:1024
	ds_read_b128 v[152:155], v2 offset:2048
	ds_read_b128 v[156:159], v2 offset:3072
	v_add_u32_e32 v2, s67, v1
	ds_read_b128 v[160:163], v2
	ds_read_b128 v[164:167], v2 offset:1024
	ds_read_b128 v[168:171], v2 offset:2048
	ds_read_b128 v[172:175], v2 offset:3072
	ds_read_b128 v[176:179], v146 offset:32768
	ds_read_b128 v[180:183], v146 offset:33792
	ds_read_b128 v[184:187], v146 offset:34816
	ds_read_b128 v[188:191], v146 offset:35840
	ds_read_b128 v[192:195], v146 offset:36864
	ds_read_b128 v[204:207], v146 offset:37888
	ds_read_b128 v[208:211], v146 offset:38912
	ds_read_b128 v[212:215], v146 offset:39936
	s_waitcnt vmcnt(8)
	s_waitcnt lgkmcnt(0)
	s_barrier
	s_setprio 1
	s_waitcnt lgkmcnt(0)
	v_mfma_f32_16x16x32_bf16 v[128:131], v[132:135], v[176:179], v[128:131]
	v_mfma_f32_16x16x32_bf16 v[124:127], v[152:155], v[176:179], v[124:127]
	v_mfma_f32_16x16x32_bf16 v[116:119], v[132:135], v[184:187], v[116:119]
	v_mfma_f32_16x16x32_bf16 v[108:111], v[152:155], v[184:187], v[108:111]
	v_mfma_f32_16x16x32_bf16 v[100:103], v[132:135], v[192:195], v[100:103]
	v_mfma_f32_16x16x32_bf16 v[92:95], v[152:155], v[192:195], v[92:95]
	v_mfma_f32_16x16x32_bf16 v[84:87], v[132:135], v[208:211], v[84:87]
	v_mfma_f32_16x16x32_bf16 v[76:79], v[152:155], v[208:211], v[76:79]
	v_mfma_f32_16x16x32_bf16 v[128:131], v[148:151], v[180:183], v[128:131]
	v_mfma_f32_16x16x32_bf16 v[124:127], v[156:159], v[180:183], v[124:127]
	v_mfma_f32_16x16x32_bf16 v[116:119], v[148:151], v[188:191], v[116:119]
	v_mfma_f32_16x16x32_bf16 v[108:111], v[156:159], v[188:191], v[108:111]
	v_mfma_f32_16x16x32_bf16 v[100:103], v[148:151], v[204:207], v[100:103]
	v_mfma_f32_16x16x32_bf16 v[92:95], v[156:159], v[204:207], v[92:95]
	v_mfma_f32_16x16x32_bf16 v[84:87], v[148:151], v[212:215], v[84:87]
	v_mfma_f32_16x16x32_bf16 v[76:79], v[156:159], v[212:215], v[76:79]
	s_setprio 0
	s_setprio 1
	v_mfma_f32_16x16x32_bf16 v[120:123], v[160:163], v[176:179], v[120:123]
	v_mfma_f32_16x16x32_bf16 v[112:115], v[168:171], v[176:179], v[112:115]
	v_mfma_f32_16x16x32_bf16 v[104:107], v[160:163], v[184:187], v[104:107]
	v_mfma_f32_16x16x32_bf16 v[96:99], v[168:171], v[184:187], v[96:99]
	v_mfma_f32_16x16x32_bf16 v[88:91], v[160:163], v[192:195], v[88:91]
	v_mfma_f32_16x16x32_bf16 v[80:83], v[168:171], v[192:195], v[80:83]
	v_mfma_f32_16x16x32_bf16 v[72:75], v[160:163], v[208:211], v[72:75]
	v_mfma_f32_16x16x32_bf16 v[68:71], v[168:171], v[208:211], v[68:71]
	v_mfma_f32_16x16x32_bf16 v[120:123], v[164:167], v[180:183], v[120:123]
	v_mfma_f32_16x16x32_bf16 v[112:115], v[172:175], v[180:183], v[112:115]
	v_mfma_f32_16x16x32_bf16 v[104:107], v[164:167], v[188:191], v[104:107]
	v_mfma_f32_16x16x32_bf16 v[96:99], v[172:175], v[188:191], v[96:99]
	v_mfma_f32_16x16x32_bf16 v[88:91], v[164:167], v[204:207], v[88:91]
	v_mfma_f32_16x16x32_bf16 v[80:83], v[172:175], v[204:207], v[80:83]
	v_mfma_f32_16x16x32_bf16 v[72:75], v[164:167], v[212:215], v[72:75]
	v_mfma_f32_16x16x32_bf16 v[68:71], v[172:175], v[212:215], v[68:71]
	s_setprio 0
	s_barrier
	s_mov_b32 m0, s66
	v_lshl_add_u64 v[144:145], v[144:145], 0, s[94:95]
	global_load_lds_dwordx4 v[144:145], off
	v_lshl_add_u64 v[144:145], v[226:227], 0, s[94:95]
	s_mov_b32 m0, s65
	s_nop 0
	global_load_lds_dwordx4 v[144:145], off
	v_lshl_add_u64 v[144:145], s[30:31], 0, v[136:137]
	s_mov_b32 m0, s75
	s_nop 0
	global_load_lds_dwordx4 v[144:145], off
	v_lshl_add_u64 v[144:145], s[30:31], 0, v[140:141]
	s_mov_b32 m0, s73
	s_nop 0
	global_load_lds_dwordx4 v[144:145], off
	v_lshl_add_u64 v[144:145], v[228:229], 0, s[94:95]
	s_mov_b32 m0, s59
	s_nop 0
	global_load_lds_dwordx4 v[144:145], off
	v_lshl_add_u64 v[144:145], v[230:231], 0, s[94:95]
	s_mov_b32 m0, s60
	s_nop 0
	global_load_lds_dwordx4 v[144:145], off
	ds_read_b128 v[176:179], v146 offset:49152
	ds_read_b128 v[180:183], v146 offset:50176
	ds_read_b128 v[184:187], v146 offset:51200
	ds_read_b128 v[188:191], v146 offset:52224
	ds_read_b128 v[192:195], v146 offset:53248
	ds_read_b128 v[204:207], v146 offset:54272
	ds_read_b128 v[208:211], v146 offset:55296
	ds_read_b128 v[212:215], v146 offset:56320
	s_waitcnt vmcnt(8)
	s_waitcnt lgkmcnt(0)
	s_barrier
	s_setprio 1
	s_waitcnt lgkmcnt(0)
	v_mfma_f32_16x16x32_bf16 v[64:67], v[132:135], v[176:179], v[64:67]
	v_mfma_f32_16x16x32_bf16 v[60:63], v[152:155], v[176:179], v[60:63]
	v_mfma_f32_16x16x32_bf16 v[52:55], v[132:135], v[184:187], v[52:55]
	v_mfma_f32_16x16x32_bf16 v[44:47], v[152:155], v[184:187], v[44:47]
	v_mfma_f32_16x16x32_bf16 v[36:39], v[132:135], v[192:195], v[36:39]
	v_mfma_f32_16x16x32_bf16 v[28:31], v[152:155], v[192:195], v[28:31]
	v_mfma_f32_16x16x32_bf16 v[20:23], v[132:135], v[208:211], v[20:23]
	v_mfma_f32_16x16x32_bf16 v[12:15], v[152:155], v[208:211], v[12:15]
	v_mfma_f32_16x16x32_bf16 v[64:67], v[148:151], v[180:183], v[64:67]
	v_mfma_f32_16x16x32_bf16 v[60:63], v[156:159], v[180:183], v[60:63]
	v_mfma_f32_16x16x32_bf16 v[52:55], v[148:151], v[188:191], v[52:55]
	v_mfma_f32_16x16x32_bf16 v[44:47], v[156:159], v[188:191], v[44:47]
	v_mfma_f32_16x16x32_bf16 v[36:39], v[148:151], v[204:207], v[36:39]
	v_mfma_f32_16x16x32_bf16 v[28:31], v[156:159], v[204:207], v[28:31]
	v_mfma_f32_16x16x32_bf16 v[20:23], v[148:151], v[212:215], v[20:23]
	v_mfma_f32_16x16x32_bf16 v[12:15], v[156:159], v[212:215], v[12:15]
	s_setprio 0
	s_setprio 1
	v_mfma_f32_16x16x32_bf16 v[56:59], v[160:163], v[176:179], v[56:59]
	v_mfma_f32_16x16x32_bf16 v[48:51], v[168:171], v[176:179], v[48:51]
	v_mfma_f32_16x16x32_bf16 v[40:43], v[160:163], v[184:187], v[40:43]
	v_mfma_f32_16x16x32_bf16 v[32:35], v[168:171], v[184:187], v[32:35]
	v_mfma_f32_16x16x32_bf16 v[24:27], v[160:163], v[192:195], v[24:27]
	v_mfma_f32_16x16x32_bf16 v[16:19], v[168:171], v[192:195], v[16:19]
	v_mfma_f32_16x16x32_bf16 v[8:11], v[160:163], v[208:211], v[8:11]
	v_mfma_f32_16x16x32_bf16 v[4:7], v[168:171], v[208:211], v[4:7]
	v_mfma_f32_16x16x32_bf16 v[56:59], v[164:167], v[180:183], v[56:59]
	v_mfma_f32_16x16x32_bf16 v[48:51], v[172:175], v[180:183], v[48:51]
	v_mfma_f32_16x16x32_bf16 v[40:43], v[164:167], v[188:191], v[40:43]
	v_mfma_f32_16x16x32_bf16 v[32:35], v[172:175], v[188:191], v[32:35]
	v_mfma_f32_16x16x32_bf16 v[24:27], v[164:167], v[204:207], v[24:27]
	v_mfma_f32_16x16x32_bf16 v[16:19], v[172:175], v[204:207], v[16:19]
	v_mfma_f32_16x16x32_bf16 v[8:11], v[164:167], v[212:215], v[8:11]
	v_mfma_f32_16x16x32_bf16 v[4:7], v[172:175], v[212:215], v[4:7]
	s_setprio 0
	s_barrier
	s_mov_b64 s[36:37], 0
	s_mov_b64 s[30:31], -1
	s_mov_b64 s[34:35], 0x100
	s_cbranch_vccz .LBB0_2674
	s_and_b64 vcc, exec, s[12:13]
	s_cbranch_vccz .LBB0_2677
	s_barrier
